# K3 prologue loads overlapped, layer1 epilogue preloads, K2 prologue W1/soff loads before feat loads
# speedup vs baseline: 1.0135x; 1.0135x over previous
_Z6k_gemmPKfS0_PKtPKjPfPt:
	s_and_b32 s3, s2, 7
	s_mul_i32 s4, s3, 31
	s_min_u32 s3, s3, 2
	s_ashr_i32 s2, s2, 3
	s_add_i32 s12, s3, s2
	s_load_dwordx2 s[8:9], s[0:1], 0x0
	s_load_dwordx2 s[4:5], s[0:1], 0x8
	s_load_dwordx2 s[38:39], s[0:1], 0x18
	s_add_i32 s12, s12, s4
	v_lshrrev_b32_e32 v164, 6, v0
	v_and_b32_e32 v1, 63, v0
	s_mul_i32 s30, s12, 0x190
	v_lshlrev_b32_e32 v165, 4, v164
	s_movk_i32 s2, 0x100
	v_cmp_gt_u32_e32 vcc, s2, v0
	s_waitcnt lgkmcnt(0)
	s_and_saveexec_b64 s[2:3], vcc
	s_cbranch_execz .Lg_a
	s_movk_i32 s10, 0x101
	v_mov_b32_e32 v184, s12
	v_mad_u32_u24 v184, v0, s10, v184
	v_ashrrev_i32_e32 v185, 31, v184
	v_lshl_add_u64 v[184:185], v[184:185], 2, s[38:39]
	global_load_dwordx2 v[184:185], v[184:185], off
.Lg_a:
	s_or_b64 exec, exec, s[2:3]
	v_add_u32_e32 v130, 0x280, v0
	v_min_u32_e32 v130, 0x3ff, v130
	v_and_b32_e32 v131, 15, v130
	v_lshlrev_b32_e32 v132, 3, v130
	v_lshrrev_b32_e32 v130, 3, v130
	v_and_b32_e32 v130, 0x78, v130
	s_movk_i32 s10, 0x180
	v_and_or_b32 v130, v132, s10, v130
	v_lshlrev_b32_e32 v131, 2, v131
	v_lshl_or_b32 v137, v130, 6, v131
	v_add_u32_e32 v138, 0x3c0, v0
	global_load_dword v130, v137, s[4:5]
	global_load_dword v131, v137, s[4:5] offset:64
	global_load_dword v132, v137, s[4:5] offset:128
	global_load_dword v133, v137, s[4:5] offset:192
	global_load_dword v134, v137, s[4:5] offset:256
	global_load_dword v135, v137, s[4:5] offset:320
	global_load_dword v136, v137, s[4:5] offset:384
	s_nop 0
	global_load_dword v137, v137, s[4:5] offset:448
	v_min_u32_e32 v140, 0x3ff, v138
	v_lshlrev_b32_e32 v141, 7, v140
	s_movk_i32 s2, 0x180f
	v_bitop3_b32 v138, v141, s2, v140 bitop3:0xc8
	v_lshlrev_b32_e32 v138, 2, v138
	v_mov_b32_e32 v139, 0
	v_lshl_add_u64 v[138:139], s[4:5], 0, v[138:139]
	s_movk_i32 s2, 0x1000
	v_add_co_u32_e64 v146, s[2:3], s2, v138
	v_and_b32_e32 v166, 15, v0
	s_nop 0
	v_addc_co_u32_e64 v147, s[2:3], 0, v139, s[2:3]
	s_movk_i32 s2, 0x1800
	s_nop 0
	v_and_or_b32 v138, v141, s2, v140
	v_mov_b32_e32 v139, 0x1fc0
	v_lshl_or_b32 v142, v138, 2, v139
	v_lshrrev_b32_e32 v139, 3, v0
	v_lshlrev_b32_e32 v138, 3, v0
	v_and_b32_e32 v139, 56, v139
	v_and_or_b32 v138, v138, s10, v139
	v_lshlrev_b32_e32 v139, 2, v166
	v_lshl_or_b32 v138, v138, 6, v139
	global_load_dword v148, v138, s[4:5] offset:448
	global_load_dword v149, v138, s[4:5] offset:384
	global_load_dword v150, v138, s[4:5] offset:320
	global_load_dword v152, v138, s[4:5] offset:256
	global_load_dword v153, v138, s[4:5] offset:192
	global_load_dword v154, v138, s[4:5] offset:128
	global_load_dword v155, v138, s[4:5] offset:64
	global_load_dword v156, v138, s[4:5]
	s_nop 0
	global_load_dword v138, v[146:147], off offset:3584
	global_load_dword v139, v[146:147], off offset:3648
	global_load_dword v140, v[146:147], off offset:3712
	global_load_dword v141, v[146:147], off offset:3776
	global_load_dword v143, v[146:147], off offset:3840
	global_load_dword v144, v[146:147], off offset:3904
	global_load_dword v145, v[146:147], off offset:3968
	s_nop 0
	global_load_dword v146, v142, s[4:5]
	v_add_u32_e32 v180, 0x140, v0
	v_and_b32_e32 v181, 15, v180
	v_lshlrev_b32_e32 v182, 3, v180
	v_lshrrev_b32_e32 v180, 3, v180
	v_and_b32_e32 v180, 0x78, v180
	v_and_or_b32 v180, v182, s10, v180
	v_lshlrev_b32_e32 v181, 2, v181
	v_lshl_or_b32 v180, v180, 6, v181
	global_load_dword v172, v180, s[4:5]
	global_load_dword v173, v180, s[4:5] offset:64
	global_load_dword v174, v180, s[4:5] offset:128
	global_load_dword v175, v180, s[4:5] offset:192
	global_load_dword v176, v180, s[4:5] offset:256
	global_load_dword v177, v180, s[4:5] offset:320
	global_load_dword v178, v180, s[4:5] offset:384
	global_load_dword v179, v180, s[4:5] offset:448
	v_add_u32_e32 v8, s30, v165
	v_min_i32_e32 v2, 0x18698, v8
	v_ashrrev_i32_e32 v3, 31, v2
	v_lshlrev_b64 v[2:3], 11, v[2:3]
	v_lshl_add_u64 v[2:3], s[8:9], 0, v[2:3]
	v_mov_b32_e32 v191, 0
	v_lshlrev_b32_e32 v190, 4, v1
	v_lshl_add_u64 v[2:3], v[2:3], 0, v[190:191]
	s_movk_i32 s2, 0x1000
	v_add_co_u32_e32 v4, vcc, s2, v2
	s_movk_i32 s3, 0x2000
	s_nop 0
	v_addc_co_u32_e32 v5, vcc, 0, v3, vcc
	v_add_co_u32_e32 v6, vcc, s3, v2
	s_movk_i32 s4, 0x3000
	s_nop 0
	v_addc_co_u32_e32 v7, vcc, 0, v3, vcc
	global_load_dwordx4 v[122:125], v[2:3], off nt
	global_load_dwordx4 v[118:121], v[2:3], off offset:1024 nt
	global_load_dwordx4 v[106:109], v[2:3], off offset:2048 nt
	global_load_dwordx4 v[102:105], v[2:3], off offset:3072 nt
	v_add_co_u32_e32 v2, vcc, s4, v2
	global_load_dwordx4 v[110:113], v[4:5], off offset:1024 nt
	global_load_dwordx4 v[98:101], v[4:5], off offset:2048 nt
	global_load_dwordx4 v[94:97], v[6:7], off nt
	global_load_dwordx4 v[90:93], v[6:7], off offset:1024 nt
	global_load_dwordx4 v[86:89], v[6:7], off offset:2048 nt
	global_load_dwordx4 v[78:81], v[6:7], off offset:3072 nt
	v_addc_co_u32_e32 v3, vcc, 0, v3, vcc
	global_load_dwordx4 v[114:117], v[4:5], off offset:3072 nt
	global_load_dwordx4 v[82:85], v[2:3], off nt
	global_load_dwordx4 v[74:77], v[2:3], off offset:1024 nt
	global_load_dwordx4 v[70:73], v[2:3], off offset:2048 nt
	global_load_dwordx4 v[126:129], v[6:7], off offset:-4096 nt
	global_load_dwordx4 v[66:69], v[2:3], off offset:3072 nt
	v_or_b32_e32 v2, 8, v8
	v_min_i32_e32 v2, 0x18698, v2
	v_ashrrev_i32_e32 v3, 31, v2
	v_lshlrev_b64 v[2:3], 11, v[2:3]
	v_lshl_add_u64 v[2:3], s[8:9], 0, v[2:3]
	v_lshl_add_u64 v[2:3], v[2:3], 0, v[190:191]
	v_add_co_u32_e32 v4, vcc, s2, v2
	global_load_dwordx4 v[58:61], v[2:3], off nt
	global_load_dwordx4 v[54:57], v[2:3], off offset:1024 nt
	global_load_dwordx4 v[50:53], v[2:3], off offset:2048 nt
	global_load_dwordx4 v[38:41], v[2:3], off offset:3072 nt
	v_addc_co_u32_e32 v5, vcc, 0, v3, vcc
	v_add_co_u32_e32 v62, vcc, s3, v2
	s_nop 1
	v_addc_co_u32_e32 v63, vcc, 0, v3, vcc
	v_add_co_u32_e32 v2, vcc, 0x3000, v2
	global_load_dwordx4 v[42:45], v[4:5], off offset:1024 nt
	global_load_dwordx4 v[34:37], v[4:5], off offset:2048 nt
	global_load_dwordx4 v[30:33], v[62:63], off nt
	global_load_dwordx4 v[26:29], v[62:63], off offset:1024 nt
	global_load_dwordx4 v[22:25], v[62:63], off offset:2048 nt
	global_load_dwordx4 v[14:17], v[62:63], off offset:3072 nt
	v_addc_co_u32_e32 v3, vcc, 0, v3, vcc
	global_load_dwordx4 v[46:49], v[4:5], off offset:3072 nt
	global_load_dwordx4 v[18:21], v[2:3], off nt
	global_load_dwordx4 v[10:13], v[2:3], off offset:1024 nt
	global_load_dwordx4 v[6:9], v[2:3], off offset:2048 nt
	s_nop 0
	global_load_dwordx4 v[62:65], v[62:63], off offset:-4096 nt
	s_nop 0
	global_load_dwordx4 v[2:5], v[2:3], off offset:3072 nt
	s_movk_i32 s2, 0x13f
	v_cmp_eq_u32_e32 vcc, s2, v0
	s_and_saveexec_b64 s[2:3], vcc
	v_mov_b32_e32 v186, 0x19440
	v_mov_b32_e32 v187, 0
	ds_write_b32 v186, v187
	s_or_b64 exec, exec, s[2:3]
	s_movk_i32 s2, 0xff
	v_cmp_lt_u32_e64 s[2:3], s2, v0
	s_and_saveexec_b64 s[6:7], s[2:3]
	s_movk_i32 s2, 0x120
	v_cmp_gt_u32_e64 s[2:3], s2, v0
	s_and_b64 exec, exec, s[2:3]
	v_lshlrev_b32_e32 v186, 2, v0
	v_add_u32_e32 v187, 0x18b40, v186
	v_add_u32_e32 v186, 0x18fc0, v186
	v_mov_b32_e32 v188, 0
	ds_write_b32 v186, v188
	ds_write_b32 v187, v188
	s_mov_b64 exec, s[6:7]
	s_movk_i32 s2, 0x100
	v_cmp_gt_u32_e32 vcc, s2, v0
	s_waitcnt vmcnt(32)
	s_and_saveexec_b64 s[2:3], vcc
	s_movk_i32 s6, 0x30d4
	v_lshlrev_b32_e32 v186, 2, v0
	v_add_u32_e32 v187, 0x18fc0, v186
	v_add_u32_e32 v186, 0x18b40, v186
	v_mad_u32_u24 v188, v0, s6, v184
	v_sub_u32_e32 v189, v185, v184
	ds_write_b32 v187, v188
	ds_write_b32 v186, v189
	s_or_b64 exec, exec, s[2:3]
	v_mov_b32_e32 v142, 0x14500
	v_lshl_add_u32 v142, v0, 4, v142
	v_cvt_pk_bf16_f32 v151, v149, v148
	v_cvt_pk_bf16_f32 v150, v152, v150
	v_cvt_pk_bf16_f32 v149, v154, v153
	v_cvt_pk_bf16_f32 v148, v156, v155
	ds_write_b128 v142, v[148:151]
	v_cvt_pk_bf16_f32 v172, v172, v173
	v_cvt_pk_bf16_f32 v173, v174, v175
	v_cvt_pk_bf16_f32 v174, v176, v177
	v_cvt_pk_bf16_f32 v175, v178, v179
	ds_write_b128 v142, v[172:175] offset:5120
	v_cvt_pk_bf16_f32 v137, v136, v137
	v_cvt_pk_bf16_f32 v136, v134, v135
	v_cvt_pk_bf16_f32 v135, v132, v133
	v_cvt_pk_bf16_f32 v134, v130, v131
	ds_write_b128 v142, v[134:137] offset:10240
	v_cmp_gt_u32_e64 s[2:3], 64, v0
	s_and_saveexec_b64 s[4:5], s[2:3]
	v_cvt_pk_bf16_f32 v133, v145, v146
	v_cvt_pk_bf16_f32 v132, v143, v144
	v_cvt_pk_bf16_f32 v131, v140, v141
	v_cvt_pk_bf16_f32 v130, v138, v139
	ds_write_b128 v142, v[130:133] offset:15360
	s_or_b64 exec, exec, s[4:5]
	s_load_dwordx2 s[26:27], s[0:1], 0x10
	s_load_dwordx2 s[24:25], s[0:1], 0x20
	s_movk_i32 s2, 0x190
	v_lshlrev_b32_e32 v130, 2, v1
	v_cmp_gt_u32_e64 s[2:3], s2, v0
	s_and_saveexec_b64 s[10:11], s[2:3]
	s_cbranch_execz .LBB1_42
	s_movk_i32 s4, 0x50
	v_sub_u32_e64 v131, s4, v0 clamp
	v_cmp_gt_u32_e64 s[4:5], s4, v0
	v_mov_b32_e32 v136, 0
	s_mov_b32 s15, 1
	v_subbrev_co_u32_e64 v131, s[6:7], 0, v131, s[4:5]
	s_mov_b32 s6, 0xcccccccd
	s_nop 0
	v_mul_hi_u32 v131, v131, s6
	v_lshrrev_b32_e32 v131, 8, v131
	v_addc_co_u32_e64 v131, s[4:5], 0, v131, s[4:5]
	v_lshrrev_b32_e32 v132, 1, v131
	v_add_u32_e32 v132, 1, v132
	v_cmp_lt_u32_e64 s[4:5], 5, v131
	s_and_saveexec_b64 s[12:13], s[4:5]
	s_cbranch_execz .LBB1_35
	v_mov_b32_e32 v134, 0x18500
	s_mov_b32 s14, 0
	v_and_b32_e32 v133, 0x1fffffc, v132
	v_lshl_add_u32 v134, v0, 2, v134
	s_mov_b64 s[16:17], 0
	v_mov_b32_e32 v135, 0
	s_mov_b32 s18, s14
	s_branch .LBB1_16

.LBB1_16:
	s_mov_b32 s19, s18
	s_or_b64 s[6:7], s[18:19], s[14:15]
	v_cmp_le_u32_e64 s[4:5], s7, v131
	v_cmp_le_u32_e64 s[6:7], s6, v131
	s_and_saveexec_b64 s[20:21], s[6:7]
	ds_write_b32 v134, v135
	s_or_b64 exec, exec, s[20:21]
	s_and_saveexec_b64 s[6:7], s[4:5]
	ds_write_b32 v134, v135 offset:1280
	s_or_b64 exec, exec, s[6:7]
	s_add_i32 s20, s18, 2
	s_mov_b32 s21, s20
	s_or_b64 s[6:7], s[20:21], s[14:15]
	v_cmp_le_u32_e64 s[4:5], s7, v131
	v_cmp_le_u32_e64 s[6:7], s6, v131
	s_and_saveexec_b64 s[22:23], s[6:7]
	ds_write_b32 v134, v135 offset:2560
	s_or_b64 exec, exec, s[22:23]
	s_and_saveexec_b64 s[6:7], s[4:5]
	ds_write_b32 v134, v135 offset:3840
	s_or_b64 exec, exec, s[6:7]
	s_add_i32 s20, s20, 2
	s_mov_b32 s21, s20
	s_or_b64 s[6:7], s[20:21], s[14:15]
	v_cmp_le_u32_e64 s[4:5], s7, v131
	v_cmp_le_u32_e64 s[6:7], s6, v131
	s_and_saveexec_b64 s[22:23], s[6:7]
	ds_write_b32 v134, v135 offset:5120
	s_or_b64 exec, exec, s[22:23]
	s_and_saveexec_b64 s[6:7], s[4:5]
	ds_write_b32 v134, v135 offset:6400
	s_or_b64 exec, exec, s[6:7]
	s_add_i32 s20, s20, 2
	s_mov_b32 s21, s20
	s_or_b64 s[6:7], s[20:21], s[14:15]
	v_cmp_le_u32_e64 s[4:5], s7, v131
	v_cmp_le_u32_e64 s[6:7], s6, v131
	s_and_saveexec_b64 s[22:23], s[6:7]
	ds_write_b32 v134, v135 offset:7680
	s_or_b64 exec, exec, s[22:23]
	s_and_saveexec_b64 s[6:7], s[4:5]
	s_cbranch_execz .LBB1_15
	ds_write_b32 v134, v135 offset:8960
	s_branch .LBB1_15
.LBB1_34:
	s_or_b64 exec, exec, s[16:17]

.LBB1_45:
	s_or_b64 exec, exec, s[0:1]
	v_lshlrev_b32_e32 v130, 2, v130
	v_mov_b32_e32 v131, 0
	v_lshlrev_b32_e32 v134, 2, v164
	v_lshl_add_u64 v[162:163], s[8:9], 0, v[130:131]
	v_mov_b32_e32 v183, v1
	v_or_b32_e32 v169, 0x18fc0, v134
	v_add_u32_e32 v130, 0x18fd4, v134
	v_add_u32_e32 v135, 0x18b68, v134
	v_add_u32_e32 v136, 0x18ffc, v134
	v_add_u32_e32 v137, 0x18b7c, v134
	v_or_b32_e32 v170, 0x18b40, v134
	v_add_u32_e32 v132, 0x18b54, v134
	v_add_u32_e32 v133, 0x18fe8, v134
	ds_read_b32 v138, v169
	ds_read_b32 v139, v170
	ds_read_b32 v140, v130
	ds_read_b32 v141, v132
	ds_read_b32 v142, v133
	ds_read_b32 v135, v135
	ds_read_b32 v136, v136
	ds_read_b32 v137, v137
	s_waitcnt lgkmcnt(7)
	v_add_u32_e32 v130, v138, v1
	s_waitcnt lgkmcnt(6)
	v_cmp_lt_u32_e64 s[18:19], v1, v139
	s_waitcnt lgkmcnt(4)
	v_cmp_lt_u32_e32 vcc, v1, v141
	s_waitcnt lgkmcnt(2)
	v_cmp_lt_u32_e64 s[8:9], v1, v135
	v_cndmask_b32_e64 v130, 0, v130, s[18:19]
	v_lshl_add_u64 v[132:133], v[130:131], 1, s[26:27]
	v_add_u32_e32 v130, v140, v1
	v_cndmask_b32_e32 v130, 0, v130, vcc
	global_load_ushort v181, v[132:133], off
	v_lshl_add_u64 v[132:133], v[130:131], 1, s[26:27]
	v_add_u32_e32 v130, v142, v1
	v_cndmask_b32_e64 v130, 0, v130, s[8:9]
	global_load_ushort v178, v[132:133], off
	v_lshl_add_u64 v[132:133], v[130:131], 1, s[26:27]
	s_waitcnt lgkmcnt(1)
	v_add_u32_e32 v130, v136, v1
	s_waitcnt lgkmcnt(0)
	v_cmp_lt_u32_e64 s[4:5], v1, v137
	global_load_ushort v176, v[132:133], off
	v_add_u32_e32 v135, 0x18ba4, v134
	v_cndmask_b32_e64 v130, 0, v130, s[4:5]
	v_lshl_add_u64 v[132:133], v[130:131], 1, s[26:27]
	global_load_ushort v172, v[132:133], off
	v_add_u32_e32 v130, 0x19010, v134
	v_add_u32_e32 v132, 0x18b90, v134
	v_add_u32_e32 v136, 0x19038, v134
	v_add_u32_e32 v137, 0x18bb8, v134
	v_add_u32_e32 v138, 0x1904c, v134
	v_add_u32_e32 v139, 0x18bcc, v134
	v_add_u32_e32 v133, 0x19024, v134
	ds_read_b32 v130, v130
	ds_read_b32 v132, v132
	ds_read_b32 v140, v133
	ds_read_b32 v135, v135
	ds_read_b32 v136, v136
	ds_read_b32 v137, v137
	ds_read_b32 v138, v138
	ds_read_b32 v139, v139
	s_waitcnt lgkmcnt(7)
	v_add_u32_e32 v130, v130, v1
	s_waitcnt lgkmcnt(6)
	v_cmp_lt_u32_e64 s[20:21], v1, v132
	s_waitcnt lgkmcnt(4)
	v_cmp_lt_u32_e64 s[16:17], v1, v135
	s_waitcnt lgkmcnt(2)
	v_cmp_lt_u32_e64 s[10:11], v1, v137
	v_cndmask_b32_e64 v130, 0, v130, s[20:21]
	v_lshl_add_u64 v[132:133], v[130:131], 1, s[26:27]
	v_add_u32_e32 v130, v140, v1
	v_cndmask_b32_e64 v130, 0, v130, s[16:17]
	global_load_ushort v182, v[132:133], off
	v_lshl_add_u64 v[132:133], v[130:131], 1, s[26:27]
	v_add_u32_e32 v130, v136, v1
	v_cndmask_b32_e64 v130, 0, v130, s[10:11]
	global_load_ushort v179, v[132:133], off
	v_lshl_add_u64 v[132:133], v[130:131], 1, s[26:27]
	s_waitcnt lgkmcnt(1)
	v_add_u32_e32 v130, v138, v1
	s_waitcnt lgkmcnt(0)
	v_cmp_lt_u32_e64 s[6:7], v1, v139
	global_load_ushort v177, v[132:133], off
	v_add_u32_e32 v135, 0x18bf4, v134
	v_cndmask_b32_e64 v130, 0, v130, s[6:7]
	v_lshl_add_u64 v[132:133], v[130:131], 1, s[26:27]
	global_load_ushort v173, v[132:133], off
	v_or_b32_e32 v130, 0x19060, v134
	v_or_b32_e32 v132, 0x18be0, v134
	v_add_u32_e32 v133, 0x19074, v134
	v_add_u32_e32 v136, 0x19088, v134
	v_add_u32_e32 v134, 0x18c08, v134
	ds_read_b32 v130, v130
	ds_read_b32 v132, v132
	ds_read_b32 v137, v133
	ds_read_b32 v135, v135
	ds_read_b32 v136, v136
	ds_read_b32 v134, v134
	s_waitcnt lgkmcnt(5)
	v_add_u32_e32 v130, v130, v1
	s_waitcnt lgkmcnt(4)
	v_cmp_lt_u32_e64 s[14:15], v1, v132
	s_waitcnt lgkmcnt(2)
	v_cmp_lt_u32_e64 s[12:13], v1, v135
	s_movk_i32 s22, 0x4100
	v_cndmask_b32_e64 v130, 0, v130, s[14:15]
	v_lshl_add_u64 v[132:133], v[130:131], 1, s[26:27]
	v_add_u32_e32 v130, v137, v1
	v_cndmask_b32_e64 v130, 0, v130, s[12:13]
	global_load_ushort v180, v[132:133], off
	v_lshl_add_u64 v[132:133], v[130:131], 1, s[26:27]
	s_waitcnt lgkmcnt(1)
	v_add_u32_e32 v130, v136, v1
	s_waitcnt lgkmcnt(0)
	v_cmp_lt_u32_e64 s[0:1], v1, v134
	global_load_ushort v175, v[132:133], off
	v_lshrrev_b32_e32 v167, 4, v1
	v_cndmask_b32_e64 v130, 0, v130, s[0:1]
	v_lshl_add_u64 v[130:131], v[130:131], 1, s[26:27]
	global_load_ushort v174, v[130:131], off
	v_lshlrev_b32_e32 v130, 3, v1
	v_mad_u32_u24 v171, v164, s22, v130
	v_mul_u32_u24_e32 v130, 0x410, v166
	v_mad_u32_u24 v130, v164, s22, v130
	v_lshlrev_b32_e32 v131, 8, v167
	v_add_u32_e32 v168, v130, v131
	s_add_i32 s33, s30, 0x50
	s_add_i32 s31, s30, 0x58
	s_waitcnt vmcnt(27)
	v_cvt_pk_bf16_f32 v106, v106, v107
	v_cvt_pk_bf16_f32 v107, v108, v109
	v_cvt_pk_bf16_f32 v102, v102, v103
	v_cvt_pk_bf16_f32 v103, v104, v105
	ds_write2_b64 v171, v[106:107], v[102:103] offset0:130 offset1:194
	v_cvt_pk_bf16_f32 v102, v126, v127
	v_cvt_pk_bf16_f32 v103, v128, v129
	v_cvt_pk_bf16_f32 v104, v110, v111
	v_cvt_pk_bf16_f32 v105, v112, v113
	v_add_u32_e32 v106, 32, v171
	v_cvt_pk_bf16_f32 v86, v86, v87
	v_cvt_pk_bf16_f32 v87, v88, v89
	v_cvt_pk_bf16_f32 v78, v78, v79
	v_cvt_pk_bf16_f32 v79, v80, v81
	v_add_u32_e32 v80, 0x50, v171
	v_cvt_pk_bf16_f32 v122, v122, v123
	v_cvt_pk_bf16_f32 v123, v124, v125
	v_cvt_pk_bf16_f32 v118, v118, v119
	v_cvt_pk_bf16_f32 v119, v120, v121
	ds_write2st64_b64 v106, v[102:103], v[104:105] offset0:4 offset1:5
	v_cvt_pk_bf16_f32 v98, v98, v99
	v_cvt_pk_bf16_f32 v99, v100, v101
	v_cvt_pk_bf16_f32 v100, v114, v115
	v_cvt_pk_bf16_f32 v101, v116, v117
	v_add_u32_e32 v102, 48, v171
	v_cvt_pk_bf16_f32 v94, v94, v95
	v_cvt_pk_bf16_f32 v95, v96, v97
	v_cvt_pk_bf16_f32 v90, v90, v91
	v_cvt_pk_bf16_f32 v91, v92, v93
	v_add_u32_e32 v92, 64, v171
	ds_write2st64_b64 v80, v[86:87], v[78:79] offset0:10 offset1:11
	v_cvt_pk_bf16_f32 v78, v82, v83
	v_cvt_pk_bf16_f32 v79, v84, v85
	v_cvt_pk_bf16_f32 v74, v74, v75
	v_cvt_pk_bf16_f32 v75, v76, v77
	v_add_u32_e32 v76, 0x60, v171
	v_cvt_pk_bf16_f32 v70, v70, v71
	v_cvt_pk_bf16_f32 v71, v72, v73
	v_cvt_pk_bf16_f32 v66, v66, v67
	v_cvt_pk_bf16_f32 v67, v68, v69
	v_add_u32_e32 v68, 0x70, v171
	ds_write2st64_b64 v171, v[122:123], v[118:119] offset1:1
	ds_write2st64_b64 v102, v[98:99], v[100:101] offset0:6 offset1:7
	ds_write2st64_b64 v92, v[94:95], v[90:91] offset0:8 offset1:9
	ds_write2st64_b64 v76, v[78:79], v[74:75] offset0:12 offset1:13
	ds_write2st64_b64 v68, v[70:71], v[66:67] offset0:14 offset1:15
	v_add_u32_e32 v66, s33, v165
	v_min_i32_e32 v66, 0x18698, v66
	v_ashrrev_i32_e32 v67, 31, v66
	v_lshlrev_b64 v[66:67], 11, v[66:67]
	v_lshl_add_u64 v[66:67], v[162:163], 0, v[66:67]
	s_movk_i32 s34, 0x1000
	v_add_co_u32_e64 v68, s[22:23], s34, v66
	s_movk_i32 s35, 0x2000
	s_nop 0
	v_addc_co_u32_e64 v69, s[22:23], 0, v67, s[22:23]
	v_add_co_u32_e64 v98, s[22:23], s35, v66
	s_movk_i32 s36, 0x3000
	s_nop 0
	v_addc_co_u32_e64 v99, s[22:23], 0, v67, s[22:23]
	global_load_dwordx4 v[146:149], v[66:67], off nt
	global_load_dwordx4 v[138:141], v[66:67], off offset:1024 nt
	global_load_dwordx4 v[126:129], v[66:67], off offset:2048 nt
	global_load_dwordx4 v[118:121], v[66:67], off offset:3072 nt
	v_add_co_u32_e64 v66, s[22:23], s36, v66
	global_load_dwordx4 v[130:133], v[68:69], off offset:1024 nt
	global_load_dwordx4 v[102:105], v[68:69], off offset:2048 nt
	global_load_dwordx4 v[94:97], v[98:99], off nt
	global_load_dwordx4 v[90:93], v[98:99], off offset:1024 nt
	global_load_dwordx4 v[86:89], v[98:99], off offset:2048 nt
	global_load_dwordx4 v[78:81], v[98:99], off offset:3072 nt
	v_addc_co_u32_e64 v67, s[22:23], 0, v67, s[22:23]
	global_load_dwordx4 v[134:137], v[68:69], off offset:3072 nt
	global_load_dwordx4 v[82:85], v[66:67], off nt
	global_load_dwordx4 v[74:77], v[66:67], off offset:1024 nt
	global_load_dwordx4 v[70:73], v[66:67], off offset:2048 nt
	global_load_dwordx4 v[158:161], v[98:99], off offset:-4096 nt
	s_nop 0
	global_load_dwordx4 v[66:69], v[66:67], off offset:3072 nt
	s_waitcnt vmcnt(27)
	v_cvt_pk_bf16_f32 v50, v50, v51
	v_cvt_pk_bf16_f32 v51, v52, v53
	v_cvt_pk_bf16_f32 v38, v38, v39
	v_cvt_pk_bf16_f32 v39, v40, v41
	v_add_u32_e32 v40, 0x90, v171
	ds_write2st64_b64 v40, v[50:51], v[38:39] offset0:18 offset1:19
	v_cvt_pk_bf16_f32 v38, v62, v63
	v_cvt_pk_bf16_f32 v39, v64, v65
	v_cvt_pk_bf16_f32 v40, v42, v43
	v_cvt_pk_bf16_f32 v41, v44, v45
	v_add_u32_e32 v42, 0xa0, v171
	v_cvt_pk_bf16_f32 v22, v22, v23
	v_cvt_pk_bf16_f32 v23, v24, v25
	v_cvt_pk_bf16_f32 v14, v14, v15
	v_cvt_pk_bf16_f32 v15, v16, v17
	v_add_u32_e32 v16, 0xd0, v171
	v_cvt_pk_bf16_f32 v58, v58, v59
	v_cvt_pk_bf16_f32 v59, v60, v61
	v_cvt_pk_bf16_f32 v54, v54, v55
	v_cvt_pk_bf16_f32 v55, v56, v57
	v_add_u32_e32 v56, 0x80, v171
	ds_write2st64_b64 v42, v[38:39], v[40:41] offset0:20 offset1:21
	v_cvt_pk_bf16_f32 v34, v34, v35
	v_cvt_pk_bf16_f32 v35, v36, v37
	v_cvt_pk_bf16_f32 v36, v46, v47
	v_cvt_pk_bf16_f32 v37, v48, v49
	v_add_u32_e32 v38, 0xb0, v171
	v_cvt_pk_bf16_f32 v30, v30, v31
	v_cvt_pk_bf16_f32 v31, v32, v33
	v_cvt_pk_bf16_f32 v26, v26, v27
	v_cvt_pk_bf16_f32 v27, v28, v29
	v_add_u32_e32 v28, 0xc0, v171
	ds_write2st64_b64 v16, v[22:23], v[14:15] offset0:26 offset1:27
	v_cvt_pk_bf16_f32 v14, v18, v19
	v_cvt_pk_bf16_f32 v15, v20, v21
	v_cvt_pk_bf16_f32 v10, v10, v11
	v_cvt_pk_bf16_f32 v11, v12, v13
	v_add_u32_e32 v12, 0xe0, v171
	v_cvt_pk_bf16_f32 v6, v6, v7
	v_cvt_pk_bf16_f32 v7, v8, v9
	v_cvt_pk_bf16_f32 v2, v2, v3
	v_cvt_pk_bf16_f32 v3, v4, v5
	v_add_u32_e32 v4, 0xf0, v171
	ds_write2st64_b64 v56, v[58:59], v[54:55] offset0:16 offset1:17
	ds_write2st64_b64 v38, v[34:35], v[36:37] offset0:22 offset1:23
	ds_write2st64_b64 v28, v[30:31], v[26:27] offset0:24 offset1:25
	ds_write2st64_b64 v12, v[14:15], v[10:11] offset0:28 offset1:29
	ds_write2st64_b64 v4, v[6:7], v[2:3] offset0:30 offset1:31
	v_add_u32_e32 v2, s31, v165
	v_min_i32_e32 v2, 0x18698, v2
	v_ashrrev_i32_e32 v3, 31, v2
	v_lshlrev_b64 v[2:3], 11, v[2:3]
	v_lshl_add_u64 v[2:3], v[162:163], 0, v[2:3]
	v_add_co_u32_e64 v4, s[22:23], s34, v2
	global_load_dwordx4 v[150:153], v[2:3], off nt
	global_load_dwordx4 v[142:145], v[2:3], off offset:1024 nt
	global_load_dwordx4 v[122:125], v[2:3], off offset:2048 nt
	global_load_dwordx4 v[110:113], v[2:3], off offset:3072 nt
	v_addc_co_u32_e64 v5, s[22:23], 0, v3, s[22:23]
	v_add_co_u32_e64 v6, s[22:23], s35, v2
	s_nop 1
	v_addc_co_u32_e64 v7, s[22:23], 0, v3, s[22:23]
	v_add_co_u32_e64 v2, s[22:23], s36, v2
	global_load_dwordx4 v[114:117], v[4:5], off offset:1024 nt
	global_load_dwordx4 v[98:101], v[4:5], off offset:2048 nt
	global_load_dwordx4 v[50:53], v[6:7], off nt
	global_load_dwordx4 v[38:41], v[6:7], off offset:1024 nt
	global_load_dwordx4 v[34:37], v[6:7], off offset:2048 nt
	global_load_dwordx4 v[26:29], v[6:7], off offset:3072 nt
	v_addc_co_u32_e64 v3, s[22:23], 0, v3, s[22:23]
	global_load_dwordx4 v[106:109], v[4:5], off offset:3072 nt
	global_load_dwordx4 v[30:33], v[2:3], off nt
	global_load_dwordx4 v[14:17], v[2:3], off offset:1024 nt
	global_load_dwordx4 v[10:13], v[2:3], off offset:2048 nt
	global_load_dwordx4 v[154:157], v[6:7], off offset:-4096 nt
	s_nop 0
	global_load_dwordx4 v[6:9], v[2:3], off offset:3072 nt
	v_mov_b32_e32 v2, 0x14500
	v_lshl_add_u32 v54, v183, 4, v2
	ds_read_b128 v[2:5], v54
	ds_read_b128 v[18:21], v54 offset:1024
	ds_read_b128 v[22:25], v168
	ds_read_b128 v[42:45], v168 offset:16
	s_waitcnt lgkmcnt(1)
	v_mfma_f32_16x16x32_bf16 v[2:5], v[2:5], v[22:25], 0
	ds_read_b128 v[22:25], v54 offset:2048
	ds_read_b128 v[46:49], v54 offset:3072
	s_waitcnt lgkmcnt(2)
	v_mfma_f32_16x16x32_bf16 v[2:5], v[18:21], v[42:45], v[2:5]
	ds_read_b128 v[18:21], v168 offset:32
	ds_read_b128 v[42:45], v168 offset:48
	s_waitcnt lgkmcnt(1)
	v_mfma_f32_16x16x32_bf16 v[2:5], v[22:25], v[18:21], v[2:5]
	s_waitcnt lgkmcnt(0)
	v_mfma_f32_16x16x32_bf16 v[2:5], v[46:49], v[42:45], v[2:5]
	ds_read_b128 v[18:21], v54 offset:4096
	ds_read_b128 v[22:25], v54 offset:5120
	ds_read_b128 v[42:45], v168 offset:64
	ds_read_b128 v[46:49], v168 offset:80
	s_waitcnt lgkmcnt(1)
	v_mfma_f32_16x16x32_bf16 v[2:5], v[18:21], v[42:45], v[2:5]
	ds_read_b128 v[18:21], v54 offset:6144
	ds_read_b128 v[42:45], v54 offset:7168
	s_waitcnt lgkmcnt(2)
	v_mfma_f32_16x16x32_bf16 v[2:5], v[22:25], v[46:49], v[2:5]
	ds_read_b128 v[22:25], v168 offset:96
	ds_read_b128 v[46:49], v168 offset:112
	s_waitcnt lgkmcnt(1)
	v_mfma_f32_16x16x32_bf16 v[2:5], v[18:21], v[22:25], v[2:5]
	s_waitcnt lgkmcnt(0)
	v_mfma_f32_16x16x32_bf16 v[2:5], v[42:45], v[46:49], v[2:5]
	ds_read_b128 v[18:21], v54 offset:8192
	ds_read_b128 v[22:25], v54 offset:9216
	ds_read_b128 v[42:45], v168 offset:128
	ds_read_b128 v[46:49], v168 offset:144
	s_waitcnt lgkmcnt(1)
	v_mfma_f32_16x16x32_bf16 v[2:5], v[18:21], v[42:45], v[2:5]
	ds_read_b128 v[18:21], v54 offset:10240
	ds_read_b128 v[42:45], v54 offset:11264
	s_waitcnt lgkmcnt(2)
	v_mfma_f32_16x16x32_bf16 v[2:5], v[22:25], v[46:49], v[2:5]
	ds_read_b128 v[22:25], v168 offset:160
	ds_read_b128 v[46:49], v168 offset:176
	s_waitcnt lgkmcnt(1)
	v_mfma_f32_16x16x32_bf16 v[2:5], v[18:21], v[22:25], v[2:5]
	s_waitcnt lgkmcnt(0)
	v_mfma_f32_16x16x32_bf16 v[2:5], v[42:45], v[46:49], v[2:5]
	ds_read_b128 v[18:21], v54 offset:12288
	ds_read_b128 v[22:25], v54 offset:13312
	ds_read_b128 v[42:45], v168 offset:192
	ds_read_b128 v[46:49], v168 offset:208
	s_waitcnt lgkmcnt(1)
	v_mfma_f32_16x16x32_bf16 v[2:5], v[18:21], v[42:45], v[2:5]
	ds_read_b128 v[18:21], v54 offset:14336
	ds_read_b128 v[42:45], v54 offset:15360
	s_waitcnt lgkmcnt(2)
	v_mfma_f32_16x16x32_bf16 v[2:5], v[22:25], v[46:49], v[2:5]
	ds_read_b128 v[22:25], v168 offset:224
	ds_read_b128 v[46:49], v168 offset:240
	s_waitcnt lgkmcnt(1)
	v_mfma_f32_16x16x32_bf16 v[2:5], v[18:21], v[22:25], v[2:5]
	s_waitcnt lgkmcnt(0)
	v_mfma_f32_16x16x32_bf16 v[2:5], v[42:45], v[46:49], v[2:5]
	s_waitcnt vmcnt(42)
	v_cmp_ne_u16_e64 s[22:23], -1, v181
	s_and_b64 s[22:23], s[18:19], s[22:23]
	s_and_saveexec_b64 s[18:19], s[22:23]
	v_and_b32_e32 v18, 0xffff, v181
	v_mov_b32_e32 v19, 0x18500
	v_lshl_add_u32 v18, v18, 2, v19
	v_mov_b32_e32 v19, 1
	ds_add_u32 v18, v19
	s_or_b64 exec, exec, s[18:19]
	v_mov_b32_e32 v18, 0xffff
	s_mov_b32 s22, 0xffff
	s_waitcnt vmcnt(41)
	v_cndmask_b32_sdwa v19, v18, v178, vcc dst_sel:DWORD dst_unused:UNUSED_PAD src0_sel:DWORD src1_sel:WORD_0
	v_cmp_ne_u32_e32 vcc, s22, v19
	s_and_saveexec_b64 s[18:19], vcc
	v_mov_b32_e32 v20, 0x18500
	v_lshl_add_u32 v19, v19, 2, v20
	v_mov_b32_e32 v20, 1
	ds_add_u32 v19, v20
	s_or_b64 exec, exec, s[18:19]
	s_mov_b64 vcc, s[8:9]
	s_waitcnt vmcnt(40)
	v_cndmask_b32_sdwa v18, v18, v176, vcc dst_sel:DWORD dst_unused:UNUSED_PAD src0_sel:DWORD src1_sel:WORD_0
	v_cmp_ne_u32_e32 vcc, s22, v18
	s_and_saveexec_b64 s[8:9], vcc
	v_mov_b32_e32 v19, 0x18500
	v_lshl_add_u32 v18, v18, 2, v19
	v_mov_b32_e32 v19, 1
	ds_add_u32 v18, v19
	s_or_b64 exec, exec, s[8:9]
	s_mov_b64 vcc, s[4:5]
	v_mov_b32_e32 v18, 0xffff
	s_mov_b32 s8, 0xffff
	s_waitcnt vmcnt(39)
	v_cndmask_b32_sdwa v19, v18, v172, vcc dst_sel:DWORD dst_unused:UNUSED_PAD src0_sel:DWORD src1_sel:WORD_0
	v_cmp_ne_u32_e32 vcc, s8, v19
	s_and_saveexec_b64 s[4:5], vcc
	v_mov_b32_e32 v20, 0x18500
	v_lshl_add_u32 v19, v19, 2, v20
	v_mov_b32_e32 v20, 1
	ds_add_u32 v19, v20
	s_or_b64 exec, exec, s[4:5]
	s_mov_b64 vcc, s[20:21]
	s_waitcnt vmcnt(38)
	v_cndmask_b32_sdwa v18, v18, v182, vcc dst_sel:DWORD dst_unused:UNUSED_PAD src0_sel:DWORD src1_sel:WORD_0
	v_cmp_ne_u32_e32 vcc, s8, v18
	s_and_saveexec_b64 s[4:5], vcc
	v_mov_b32_e32 v19, 0x18500
	v_lshl_add_u32 v18, v18, 2, v19
	v_mov_b32_e32 v19, 1
	ds_add_u32 v18, v19
	s_or_b64 exec, exec, s[4:5]
	s_mov_b64 vcc, s[16:17]
	v_mov_b32_e32 v18, 0xffff
	s_waitcnt vmcnt(37)
	v_cndmask_b32_sdwa v19, v18, v179, vcc dst_sel:DWORD dst_unused:UNUSED_PAD src0_sel:DWORD src1_sel:WORD_0
	v_cmp_ne_u32_e32 vcc, s8, v19
	s_and_saveexec_b64 s[4:5], vcc
	v_mov_b32_e32 v20, 0x18500
	v_lshl_add_u32 v19, v19, 2, v20
	v_mov_b32_e32 v20, 1
	ds_add_u32 v19, v20
	s_or_b64 exec, exec, s[4:5]
	s_mov_b64 vcc, s[10:11]
	s_waitcnt vmcnt(36)
	v_cndmask_b32_sdwa v18, v18, v177, vcc dst_sel:DWORD dst_unused:UNUSED_PAD src0_sel:DWORD src1_sel:WORD_0
	v_cmp_ne_u32_e32 vcc, s8, v18
	s_and_saveexec_b64 s[4:5], vcc
	v_mov_b32_e32 v19, 0x18500
	v_lshl_add_u32 v18, v18, 2, v19
	v_mov_b32_e32 v19, 1
	ds_add_u32 v18, v19
	s_or_b64 exec, exec, s[4:5]
	s_mov_b64 vcc, s[6:7]
	v_mov_b32_e32 v18, 0xffff
	s_mov_b32 s6, 0xffff
	s_waitcnt vmcnt(35)
	v_cndmask_b32_sdwa v19, v18, v173, vcc dst_sel:DWORD dst_unused:UNUSED_PAD src0_sel:DWORD src1_sel:WORD_0
	v_cmp_ne_u32_e32 vcc, s6, v19
	s_and_saveexec_b64 s[4:5], vcc
	v_mov_b32_e32 v20, 0x18500
	v_lshl_add_u32 v19, v19, 2, v20
	v_mov_b32_e32 v20, 1
	ds_add_u32 v19, v20
	s_or_b64 exec, exec, s[4:5]
	s_mov_b64 vcc, s[14:15]
	s_waitcnt vmcnt(34)
	v_cndmask_b32_sdwa v18, v18, v180, vcc dst_sel:DWORD dst_unused:UNUSED_PAD src0_sel:DWORD src1_sel:WORD_0
	v_cmp_ne_u32_e32 vcc, s6, v18
	s_and_saveexec_b64 s[4:5], vcc
	v_mov_b32_e32 v19, 0x18500
	v_lshl_add_u32 v18, v18, 2, v19
	v_mov_b32_e32 v19, 1
	ds_add_u32 v18, v19
	s_or_b64 exec, exec, s[4:5]
	s_mov_b64 vcc, s[12:13]
	v_mov_b32_e32 v18, 0xffff
	s_waitcnt vmcnt(33)
	v_cndmask_b32_sdwa v19, v18, v175, vcc dst_sel:DWORD dst_unused:UNUSED_PAD src0_sel:DWORD src1_sel:WORD_0
	v_cmp_ne_u32_e32 vcc, s6, v19
	s_and_saveexec_b64 s[4:5], vcc
	v_mov_b32_e32 v20, 0x18500
	v_lshl_add_u32 v19, v19, 2, v20
	v_mov_b32_e32 v20, 1
	ds_add_u32 v19, v20
	s_or_b64 exec, exec, s[4:5]
	s_mov_b64 vcc, s[0:1]
	s_waitcnt vmcnt(32)
	v_cndmask_b32_sdwa v18, v18, v174, vcc dst_sel:DWORD dst_unused:UNUSED_PAD src0_sel:DWORD src1_sel:WORD_0
	v_cmp_ne_u32_e32 vcc, s6, v18
	s_and_saveexec_b64 s[0:1], vcc
	v_mov_b32_e32 v19, 0x18500
	v_lshl_add_u32 v18, v18, 2, v19
	v_mov_b32_e32 v19, 1
	ds_add_u32 v18, v19
	s_or_b64 exec, exec, s[0:1]
	v_mov_b32_e32 v183, v1
	ds_read2_b32 v[18:19], v169 offset0:55 offset1:60
	ds_read2_b32 v[20:21], v170 offset0:55 offset1:60
	ds_read2_b32 v[22:23], v170 offset0:65 offset1:70
	ds_read2_b32 v[24:25], v169 offset0:65 offset1:70
	v_mov_b32_e32 v43, 0
	s_waitcnt lgkmcnt(3)
	v_add_u32_e32 v18, v18, v1
	s_waitcnt lgkmcnt(2)
	v_cmp_lt_u32_e64 s[20:21], v1, v20
	s_waitcnt lgkmcnt(1)
	v_cmp_lt_u32_e64 s[16:17], v1, v22
	s_waitcnt lgkmcnt(0)
	v_add_u32_e32 v20, v24, v1
	v_add_u32_e32 v22, v25, v1
	ds_read2_b32 v[24:25], v169 offset0:75 offset1:80
	ds_read2_b32 v[46:47], v170 offset0:75 offset1:80
	v_cndmask_b32_e64 v42, 0, v18, s[20:21]
	v_add_u32_e32 v18, v19, v1
	v_cmp_lt_u32_e32 vcc, v1, v21
	v_lshl_add_u64 v[44:45], v[42:43], 1, s[26:27]
	v_cmp_lt_u32_e64 s[18:19], v1, v23
	v_cndmask_b32_e32 v42, 0, v18, vcc
	v_lshl_add_u64 v[18:19], v[42:43], 1, s[26:27]
	v_cndmask_b32_e64 v42, 0, v20, s[16:17]
	v_lshl_add_u64 v[20:21], v[42:43], 1, s[26:27]
	v_cndmask_b32_e64 v42, 0, v22, s[18:19]
	s_waitcnt lgkmcnt(1)
	v_add_u32_e32 v24, v24, v1
	s_waitcnt lgkmcnt(0)
	v_cmp_lt_u32_e64 s[12:13], v1, v46
	v_lshl_add_u64 v[22:23], v[42:43], 1, s[26:27]
	v_cmp_lt_u32_e64 s[14:15], v1, v47
	v_cndmask_b32_e64 v42, 0, v24, s[12:13]
	v_lshl_add_u64 v[48:49], v[42:43], 1, s[26:27]
	v_add_u32_e32 v42, v25, v1
	ds_read2_b32 v[24:25], v169 offset0:85 offset1:90
	ds_read2_b32 v[54:55], v170 offset0:85 offset1:90
	v_cndmask_b32_e64 v42, 0, v42, s[14:15]
	v_lshl_add_u64 v[46:47], v[42:43], 1, s[26:27]
	s_waitcnt lgkmcnt(1)
	v_add_u32_e32 v24, v24, v1
	s_waitcnt lgkmcnt(0)
	v_cmp_lt_u32_e64 s[10:11], v1, v54
	v_cmp_lt_u32_e64 s[4:5], v1, v55
	ds_read2_b32 v[54:55], v169 offset0:95 offset1:100
	ds_read2_b32 v[58:59], v170 offset0:95 offset1:100
	v_cndmask_b32_e64 v42, 0, v24, s[10:11]
	v_add_u32_e32 v24, v25, v1
	v_lshl_add_u64 v[56:57], v[42:43], 1, s[26:27]
	v_cndmask_b32_e64 v42, 0, v24, s[4:5]
	v_lshl_add_u64 v[24:25], v[42:43], 1, s[26:27]
	global_load_ushort v182, v[44:45], off
	global_load_ushort v181, v[18:19], off
	global_load_ushort v180, v[20:21], off
	global_load_ushort v179, v[22:23], off
	global_load_ushort v178, v[48:49], off
	global_load_ushort v177, v[46:47], off
	global_load_ushort v176, v[56:57], off
	global_load_ushort v174, v[24:25], off
	ds_read_b32 v22, v169 offset:420
	ds_read_b32 v23, v170 offset:420
	s_waitcnt lgkmcnt(3)
	v_add_u32_e32 v18, v54, v1
	s_waitcnt lgkmcnt(2)
	v_cmp_lt_u32_e64 s[6:7], v1, v58
	v_add_u32_e32 v20, v55, v1
	v_cmp_lt_u32_e64 s[8:9], v1, v59
	v_cndmask_b32_e64 v42, 0, v18, s[6:7]
	v_lshl_add_u64 v[18:19], v[42:43], 1, s[26:27]
	v_cndmask_b32_e64 v42, 0, v20, s[8:9]
	s_waitcnt lgkmcnt(1)
	v_add_u32_e32 v22, v22, v1
	s_waitcnt lgkmcnt(0)
	v_cmp_lt_u32_e64 s[0:1], v1, v23
	v_lshl_add_u64 v[20:21], v[42:43], 1, s[26:27]
	s_nop 0
	v_cndmask_b32_e64 v42, 0, v22, s[0:1]
	v_lshl_add_u64 v[22:23], v[42:43], 1, s[26:27]
	global_load_ushort v175, v[18:19], off
	global_load_ushort v173, v[20:21], off
	global_load_ushort v172, v[22:23], off
	s_waitcnt vmcnt(42)
	v_cvt_pk_bf16_f32 v18, v146, v147
	v_cvt_pk_bf16_f32 v19, v148, v149
	s_waitcnt vmcnt(41)
	v_cvt_pk_bf16_f32 v20, v138, v139
	v_cvt_pk_bf16_f32 v21, v140, v141
	ds_write2st64_b64 v171, v[18:19], v[20:21] offset1:1
	s_waitcnt vmcnt(40)
	v_cvt_pk_bf16_f32 v18, v126, v127
	v_cvt_pk_bf16_f32 v19, v128, v129
	s_waitcnt vmcnt(39)
	v_cvt_pk_bf16_f32 v20, v118, v119
	v_cvt_pk_bf16_f32 v21, v120, v121
	ds_write2_b64 v171, v[18:19], v[20:21] offset0:130 offset1:194
	s_waitcnt vmcnt(28)
	v_cvt_pk_bf16_f32 v18, v158, v159
	v_cvt_pk_bf16_f32 v19, v160, v161
	v_cvt_pk_bf16_f32 v20, v130, v131
	v_cvt_pk_bf16_f32 v21, v132, v133
	v_add_u32_e32 v22, 32, v171
	ds_write2st64_b64 v22, v[18:19], v[20:21] offset0:4 offset1:5
	v_cvt_pk_bf16_f32 v18, v102, v103
	v_cvt_pk_bf16_f32 v19, v104, v105
	v_cvt_pk_bf16_f32 v20, v134, v135
	v_cvt_pk_bf16_f32 v21, v136, v137
	v_add_u32_e32 v22, 48, v171
	ds_write2st64_b64 v22, v[18:19], v[20:21] offset0:6 offset1:7
	v_cvt_pk_bf16_f32 v18, v94, v95
	v_cvt_pk_bf16_f32 v19, v96, v97
	v_cvt_pk_bf16_f32 v20, v90, v91
	v_cvt_pk_bf16_f32 v21, v92, v93
	v_add_u32_e32 v22, 64, v171
	ds_write2st64_b64 v22, v[18:19], v[20:21] offset0:8 offset1:9
	v_cvt_pk_bf16_f32 v18, v86, v87
	v_cvt_pk_bf16_f32 v19, v88, v89
	v_cvt_pk_bf16_f32 v20, v78, v79
	v_cvt_pk_bf16_f32 v21, v80, v81
	v_add_u32_e32 v22, 0x50, v171
	ds_write2st64_b64 v22, v[18:19], v[20:21] offset0:10 offset1:11
	v_cvt_pk_bf16_f32 v18, v82, v83
	v_cvt_pk_bf16_f32 v19, v84, v85
	v_cvt_pk_bf16_f32 v20, v74, v75
	v_cvt_pk_bf16_f32 v21, v76, v77
	v_add_u32_e32 v22, 0x60, v171
	ds_write2st64_b64 v22, v[18:19], v[20:21] offset0:12 offset1:13
	v_cvt_pk_bf16_f32 v18, v70, v71
	v_cvt_pk_bf16_f32 v19, v72, v73
	s_waitcnt vmcnt(27)
	v_cvt_pk_bf16_f32 v20, v66, v67
	v_cvt_pk_bf16_f32 v21, v68, v69
	v_add_u32_e32 v22, 0x70, v171
	ds_write2st64_b64 v22, v[18:19], v[20:21] offset0:14 offset1:15
	v_mov_b32_e32 v18, 0x50
	v_lshl_add_u32 v158, v164, 4, v18
	v_add_u32_e32 v18, s33, v158
	v_min_i32_e32 v18, 0x18698, v18
	v_ashrrev_i32_e32 v19, 31, v18
	v_lshlrev_b64 v[18:19], 11, v[18:19]
	v_lshl_add_u64 v[18:19], v[162:163], 0, v[18:19]
	v_add_co_u32_e64 v20, s[22:23], s34, v18
	global_load_dwordx4 v[134:137], v[18:19], off nt
	global_load_dwordx4 v[130:133], v[18:19], off offset:1024 nt
	global_load_dwordx4 v[102:105], v[18:19], off offset:2048 nt
	global_load_dwordx4 v[90:93], v[18:19], off offset:3072 nt
	v_addc_co_u32_e64 v21, s[22:23], 0, v19, s[22:23]
	v_add_co_u32_e64 v66, s[22:23], s35, v18
	s_nop 1
	v_addc_co_u32_e64 v67, s[22:23], 0, v19, s[22:23]
	v_add_co_u32_e64 v18, s[22:23], s36, v18
	global_load_dwordx4 v[118:121], v[20:21], off offset:1024 nt
	global_load_dwordx4 v[78:81], v[20:21], off offset:2048 nt
	global_load_dwordx4 v[74:77], v[66:67], off nt
	global_load_dwordx4 v[62:65], v[66:67], off offset:1024 nt
	global_load_dwordx4 v[58:61], v[66:67], off offset:2048 nt
	global_load_dwordx4 v[46:49], v[66:67], off offset:3072 nt
	v_addc_co_u32_e64 v19, s[22:23], 0, v19, s[22:23]
	global_load_dwordx4 v[126:129], v[20:21], off offset:3072 nt
	global_load_dwordx4 v[54:57], v[18:19], off nt
	global_load_dwordx4 v[42:45], v[18:19], off offset:1024 nt
	global_load_dwordx4 v[22:25], v[18:19], off offset:2048 nt
	global_load_dwordx4 v[146:149], v[66:67], off offset:-4096 nt
	s_nop 0
	global_load_dwordx4 v[18:21], v[18:19], off offset:3072 nt
	s_waitcnt vmcnt(42)
	v_cvt_pk_bf16_f32 v66, v150, v151
	v_cvt_pk_bf16_f32 v67, v152, v153
	s_waitcnt vmcnt(41)
	v_cvt_pk_bf16_f32 v68, v142, v143
	v_cvt_pk_bf16_f32 v69, v144, v145
	v_add_u32_e32 v70, 0x80, v171
	ds_write2st64_b64 v70, v[66:67], v[68:69] offset0:16 offset1:17
	s_waitcnt vmcnt(40)
	v_cvt_pk_bf16_f32 v66, v122, v123
	v_cvt_pk_bf16_f32 v67, v124, v125
	s_waitcnt vmcnt(39)
	v_cvt_pk_bf16_f32 v68, v110, v111
	v_cvt_pk_bf16_f32 v69, v112, v113
	v_add_u32_e32 v70, 0x90, v171
	ds_write2st64_b64 v70, v[66:67], v[68:69] offset0:18 offset1:19
	s_waitcnt vmcnt(28)
	v_cvt_pk_bf16_f32 v66, v154, v155
	v_cvt_pk_bf16_f32 v67, v156, v157
	v_cvt_pk_bf16_f32 v68, v114, v115
	v_cvt_pk_bf16_f32 v69, v116, v117
	v_add_u32_e32 v70, 0xa0, v171
	v_cvt_pk_bf16_f32 v34, v34, v35
	v_cvt_pk_bf16_f32 v35, v36, v37
	v_cvt_pk_bf16_f32 v26, v26, v27
	v_cvt_pk_bf16_f32 v27, v28, v29
	v_add_u32_e32 v28, 0xd0, v171
	ds_write2st64_b64 v70, v[66:67], v[68:69] offset0:20 offset1:21
	v_cvt_pk_bf16_f32 v66, v98, v99
	v_cvt_pk_bf16_f32 v67, v100, v101
	v_cvt_pk_bf16_f32 v68, v106, v107
	v_cvt_pk_bf16_f32 v69, v108, v109
	v_add_u32_e32 v70, 0xb0, v171
	v_cvt_pk_bf16_f32 v50, v50, v51
	v_cvt_pk_bf16_f32 v51, v52, v53
	v_cvt_pk_bf16_f32 v38, v38, v39
	v_cvt_pk_bf16_f32 v39, v40, v41
	v_add_u32_e32 v40, 0xc0, v171
	ds_write2st64_b64 v28, v[34:35], v[26:27] offset0:26 offset1:27
	v_cvt_pk_bf16_f32 v26, v30, v31
	v_cvt_pk_bf16_f32 v27, v32, v33
	v_cvt_pk_bf16_f32 v14, v14, v15
	v_cvt_pk_bf16_f32 v15, v16, v17
	v_add_u32_e32 v16, 0xe0, v171
	v_cvt_pk_bf16_f32 v10, v10, v11
	v_cvt_pk_bf16_f32 v11, v12, v13
	s_waitcnt vmcnt(27)
	v_cvt_pk_bf16_f32 v6, v6, v7
	v_cvt_pk_bf16_f32 v7, v8, v9
	v_add_u32_e32 v8, 0xf0, v171
	ds_write2st64_b64 v70, v[66:67], v[68:69] offset0:22 offset1:23
	ds_write2st64_b64 v40, v[50:51], v[38:39] offset0:24 offset1:25
	ds_write2st64_b64 v16, v[26:27], v[14:15] offset0:28 offset1:29
	ds_write2st64_b64 v8, v[10:11], v[6:7] offset0:30 offset1:31
	v_add_u32_e32 v6, s31, v158
	v_min_i32_e32 v6, 0x18698, v6
	v_ashrrev_i32_e32 v7, 31, v6
	v_lshlrev_b64 v[6:7], 11, v[6:7]
	v_lshl_add_u64 v[6:7], v[162:163], 0, v[6:7]
	v_add_co_u32_e64 v8, s[22:23], s34, v6
	global_load_dwordx4 v[138:141], v[6:7], off nt
	global_load_dwordx4 v[114:117], v[6:7], off offset:1024 nt
	global_load_dwordx4 v[106:109], v[6:7], off offset:2048 nt
	global_load_dwordx4 v[94:97], v[6:7], off offset:3072 nt
	v_addc_co_u32_e64 v9, s[22:23], 0, v7, s[22:23]
	v_add_co_u32_e64 v10, s[22:23], s35, v6
	s_nop 1
	v_addc_co_u32_e64 v11, s[22:23], 0, v7, s[22:23]
	v_add_co_u32_e64 v6, s[22:23], s36, v6
	global_load_dwordx4 v[98:101], v[8:9], off offset:1024 nt
	global_load_dwordx4 v[82:85], v[8:9], off offset:2048 nt
	global_load_dwordx4 v[70:73], v[10:11], off nt
	global_load_dwordx4 v[66:69], v[10:11], off offset:1024 nt
	global_load_dwordx4 v[50:53], v[10:11], off offset:2048 nt
	global_load_dwordx4 v[34:37], v[10:11], off offset:3072 nt
	v_addc_co_u32_e64 v7, s[22:23], 0, v7, s[22:23]
	global_load_dwordx4 v[86:89], v[8:9], off offset:3072 nt
	global_load_dwordx4 v[38:41], v[6:7], off nt
	global_load_dwordx4 v[26:29], v[6:7], off offset:1024 nt
	global_load_dwordx4 v[14:17], v[6:7], off offset:2048 nt
	global_load_dwordx4 v[142:145], v[10:11], off offset:-4096 nt
	s_nop 0
	global_load_dwordx4 v[10:13], v[6:7], off offset:3072 nt
	v_mov_b32_e32 v6, 0x14500
	v_lshl_add_u32 v154, v183, 4, v6
	ds_read_b128 v[6:9], v154
	ds_read_b128 v[30:33], v154 offset:1024
	ds_read_b128 v[110:113], v168
	ds_read_b128 v[122:125], v168 offset:16
	s_waitcnt lgkmcnt(1)
	v_mfma_f32_16x16x32_bf16 v[6:9], v[6:9], v[110:113], 0
	ds_read_b128 v[110:113], v154 offset:2048
	ds_read_b128 v[150:153], v154 offset:3072
	s_waitcnt lgkmcnt(2)
	v_mfma_f32_16x16x32_bf16 v[6:9], v[30:33], v[122:125], v[6:9]
	ds_read_b128 v[30:33], v168 offset:32
	ds_read_b128 v[122:125], v168 offset:48
	s_waitcnt lgkmcnt(1)
	v_mfma_f32_16x16x32_bf16 v[6:9], v[110:113], v[30:33], v[6:9]
	s_waitcnt lgkmcnt(0)
	v_mfma_f32_16x16x32_bf16 v[6:9], v[150:153], v[122:125], v[6:9]
	ds_read_b128 v[30:33], v154 offset:4096
	ds_read_b128 v[110:113], v154 offset:5120
	ds_read_b128 v[122:125], v168 offset:64
	ds_read_b128 v[150:153], v168 offset:80
	s_waitcnt lgkmcnt(1)
	v_mfma_f32_16x16x32_bf16 v[6:9], v[30:33], v[122:125], v[6:9]
	ds_read_b128 v[30:33], v154 offset:6144
	ds_read_b128 v[122:125], v154 offset:7168
	s_waitcnt lgkmcnt(2)
	v_mfma_f32_16x16x32_bf16 v[6:9], v[110:113], v[150:153], v[6:9]
	ds_read_b128 v[110:113], v168 offset:96
	ds_read_b128 v[150:153], v168 offset:112
	s_waitcnt lgkmcnt(1)
	v_mfma_f32_16x16x32_bf16 v[6:9], v[30:33], v[110:113], v[6:9]
	s_waitcnt lgkmcnt(0)
	v_mfma_f32_16x16x32_bf16 v[6:9], v[122:125], v[150:153], v[6:9]
	ds_read_b128 v[30:33], v154 offset:8192
	ds_read_b128 v[110:113], v154 offset:9216
	ds_read_b128 v[122:125], v168 offset:128
	ds_read_b128 v[150:153], v168 offset:144
	s_waitcnt lgkmcnt(1)
	v_mfma_f32_16x16x32_bf16 v[6:9], v[30:33], v[122:125], v[6:9]
	ds_read_b128 v[30:33], v154 offset:10240
	ds_read_b128 v[122:125], v154 offset:11264
	s_waitcnt lgkmcnt(2)
	v_mfma_f32_16x16x32_bf16 v[6:9], v[110:113], v[150:153], v[6:9]
	ds_read_b128 v[110:113], v168 offset:160
	ds_read_b128 v[150:153], v168 offset:176
	s_waitcnt lgkmcnt(1)
	v_mfma_f32_16x16x32_bf16 v[6:9], v[30:33], v[110:113], v[6:9]
	s_waitcnt lgkmcnt(0)
	v_mfma_f32_16x16x32_bf16 v[6:9], v[122:125], v[150:153], v[6:9]
	ds_read_b128 v[30:33], v154 offset:12288
	ds_read_b128 v[110:113], v154 offset:13312
	ds_read_b128 v[122:125], v168 offset:192
	ds_read_b128 v[150:153], v168 offset:208
	s_waitcnt lgkmcnt(1)
	v_mfma_f32_16x16x32_bf16 v[6:9], v[30:33], v[122:125], v[6:9]
	ds_read_b128 v[30:33], v154 offset:14336
	ds_read_b128 v[122:125], v154 offset:15360
	s_waitcnt lgkmcnt(2)
	v_mfma_f32_16x16x32_bf16 v[6:9], v[110:113], v[150:153], v[6:9]
	ds_read_b128 v[110:113], v168 offset:224
	ds_read_b128 v[150:153], v168 offset:240
	s_waitcnt lgkmcnt(1)
	v_mfma_f32_16x16x32_bf16 v[6:9], v[30:33], v[110:113], v[6:9]
	s_waitcnt lgkmcnt(0)
	v_mfma_f32_16x16x32_bf16 v[6:9], v[122:125], v[150:153], v[6:9]
	s_waitcnt vmcnt(42)
	v_cmp_ne_u16_e64 s[22:23], -1, v182
	s_and_b64 s[22:23], s[20:21], s[22:23]
	s_and_saveexec_b64 s[20:21], s[22:23]
	v_and_b32_e32 v30, 0xffff, v182
	v_mov_b32_e32 v31, 0x18500
	v_lshl_add_u32 v30, v30, 2, v31
	v_mov_b32_e32 v31, 1
	ds_add_u32 v30, v31
	s_or_b64 exec, exec, s[20:21]
	v_mov_b32_e32 v30, 0xffff
	s_mov_b32 s22, 0xffff
	s_waitcnt vmcnt(41)
	v_cndmask_b32_sdwa v31, v30, v181, vcc dst_sel:DWORD dst_unused:UNUSED_PAD src0_sel:DWORD src1_sel:WORD_0
	v_cmp_ne_u32_e32 vcc, s22, v31
	s_and_saveexec_b64 s[20:21], vcc
	v_mov_b32_e32 v32, 0x18500
	v_lshl_add_u32 v31, v31, 2, v32
	v_mov_b32_e32 v32, 1
	ds_add_u32 v31, v32
	s_or_b64 exec, exec, s[20:21]
	s_mov_b64 vcc, s[16:17]
	s_waitcnt vmcnt(40)
	v_cndmask_b32_sdwa v30, v30, v180, vcc dst_sel:DWORD dst_unused:UNUSED_PAD src0_sel:DWORD src1_sel:WORD_0
	v_cmp_ne_u32_e32 vcc, s22, v30
	s_and_saveexec_b64 s[16:17], vcc
	v_mov_b32_e32 v31, 0x18500
	v_lshl_add_u32 v30, v30, 2, v31
	v_mov_b32_e32 v31, 1
	ds_add_u32 v30, v31
	s_or_b64 exec, exec, s[16:17]
	s_mov_b64 vcc, s[18:19]
	v_mov_b32_e32 v30, 0xffff
	s_mov_b32 s18, 0xffff
	s_waitcnt vmcnt(39)
	v_cndmask_b32_sdwa v31, v30, v179, vcc dst_sel:DWORD dst_unused:UNUSED_PAD src0_sel:DWORD src1_sel:WORD_0
	v_cmp_ne_u32_e32 vcc, s18, v31
	s_and_saveexec_b64 s[16:17], vcc
	v_mov_b32_e32 v32, 0x18500
	v_lshl_add_u32 v31, v31, 2, v32
	v_mov_b32_e32 v32, 1
	ds_add_u32 v31, v32
	s_or_b64 exec, exec, s[16:17]
	s_mov_b64 vcc, s[12:13]
	s_waitcnt vmcnt(38)
	v_cndmask_b32_sdwa v30, v30, v178, vcc dst_sel:DWORD dst_unused:UNUSED_PAD src0_sel:DWORD src1_sel:WORD_0
	v_cmp_ne_u32_e32 vcc, s18, v30
	s_and_saveexec_b64 s[12:13], vcc
	v_mov_b32_e32 v31, 0x18500
	v_lshl_add_u32 v30, v30, 2, v31
	v_mov_b32_e32 v31, 1
	ds_add_u32 v30, v31
	s_or_b64 exec, exec, s[12:13]
	s_mov_b64 vcc, s[14:15]
	v_mov_b32_e32 v30, 0xffff
	s_mov_b32 s14, 0xffff
	s_waitcnt vmcnt(37)
	v_cndmask_b32_sdwa v31, v30, v177, vcc dst_sel:DWORD dst_unused:UNUSED_PAD src0_sel:DWORD src1_sel:WORD_0
	v_cmp_ne_u32_e32 vcc, s14, v31
	s_and_saveexec_b64 s[12:13], vcc
	v_mov_b32_e32 v32, 0x18500
	v_lshl_add_u32 v31, v31, 2, v32
	v_mov_b32_e32 v32, 1
	ds_add_u32 v31, v32
	s_or_b64 exec, exec, s[12:13]
	s_mov_b64 vcc, s[10:11]
	s_waitcnt vmcnt(36)
	v_cndmask_b32_sdwa v30, v30, v176, vcc dst_sel:DWORD dst_unused:UNUSED_PAD src0_sel:DWORD src1_sel:WORD_0
	v_cmp_ne_u32_e32 vcc, s14, v30
	s_and_saveexec_b64 s[10:11], vcc
	v_mov_b32_e32 v31, 0x18500
	v_lshl_add_u32 v30, v30, 2, v31
	v_mov_b32_e32 v31, 1
	ds_add_u32 v30, v31
	s_or_b64 exec, exec, s[10:11]
	s_mov_b64 vcc, s[4:5]
	v_mov_b32_e32 v30, 0xffff
	s_mov_b32 s10, 0xffff
	s_waitcnt vmcnt(35)
	v_cndmask_b32_sdwa v31, v30, v174, vcc dst_sel:DWORD dst_unused:UNUSED_PAD src0_sel:DWORD src1_sel:WORD_0
	v_cmp_ne_u32_e32 vcc, s10, v31
	s_and_saveexec_b64 s[4:5], vcc
	v_mov_b32_e32 v32, 0x18500
	v_lshl_add_u32 v31, v31, 2, v32
	v_mov_b32_e32 v32, 1
	ds_add_u32 v31, v32
	s_or_b64 exec, exec, s[4:5]
	s_mov_b64 vcc, s[6:7]
	s_waitcnt vmcnt(34)
	v_cndmask_b32_sdwa v30, v30, v175, vcc dst_sel:DWORD dst_unused:UNUSED_PAD src0_sel:DWORD src1_sel:WORD_0
	v_cmp_ne_u32_e32 vcc, s10, v30
	s_and_saveexec_b64 s[4:5], vcc
	v_mov_b32_e32 v31, 0x18500
	v_lshl_add_u32 v30, v30, 2, v31
	v_mov_b32_e32 v31, 1
	ds_add_u32 v30, v31
	s_or_b64 exec, exec, s[4:5]
	s_mov_b64 vcc, s[8:9]
	v_mov_b32_e32 v30, 0xffff
	s_mov_b32 s6, 0xffff
	s_waitcnt vmcnt(33)
	v_cndmask_b32_sdwa v31, v30, v173, vcc dst_sel:DWORD dst_unused:UNUSED_PAD src0_sel:DWORD src1_sel:WORD_0
	v_cmp_ne_u32_e32 vcc, s6, v31
	s_and_saveexec_b64 s[4:5], vcc
	v_mov_b32_e32 v32, 0x18500
	v_lshl_add_u32 v31, v31, 2, v32
	v_mov_b32_e32 v32, 1
	ds_add_u32 v31, v32
	s_or_b64 exec, exec, s[4:5]
	s_mov_b64 vcc, s[0:1]
	s_waitcnt vmcnt(32)
	v_cndmask_b32_sdwa v30, v30, v172, vcc dst_sel:DWORD dst_unused:UNUSED_PAD src0_sel:DWORD src1_sel:WORD_0
	v_cmp_ne_u32_e32 vcc, s6, v30
	s_and_saveexec_b64 s[0:1], vcc
	v_mov_b32_e32 v31, 0x18500
	v_lshl_add_u32 v30, v30, 2, v31
	v_mov_b32_e32 v31, 1
	ds_add_u32 v30, v31
	s_or_b64 exec, exec, s[0:1]
	v_mov_b32_e32 v173, v1
	ds_read2_b32 v[30:31], v169 offset0:110 offset1:115
	ds_read2_b32 v[32:33], v170 offset0:110 offset1:115
	ds_read2_b32 v[110:111], v170 offset0:120 offset1:125
	ds_read2_b32 v[112:113], v169 offset0:120 offset1:125
	v_mov_b32_e32 v123, 0
	s_waitcnt lgkmcnt(3)
	v_add_u32_e32 v30, v30, v1
	s_waitcnt lgkmcnt(2)
	v_cmp_lt_u32_e64 s[20:21], v1, v32
	s_waitcnt lgkmcnt(1)
	v_cmp_lt_u32_e64 s[16:17], v1, v110
	s_waitcnt lgkmcnt(0)
	v_add_u32_e32 v32, v112, v1
	v_add_u32_e32 v110, v113, v1
	ds_read2_b32 v[112:113], v169 offset0:130 offset1:135
	ds_read2_b32 v[150:151], v170 offset0:130 offset1:135
	v_cndmask_b32_e64 v122, 0, v30, s[20:21]
	v_add_u32_e32 v30, v31, v1
	v_cmp_lt_u32_e32 vcc, v1, v33
	v_lshl_add_u64 v[124:125], v[122:123], 1, s[26:27]
	v_cmp_lt_u32_e64 s[18:19], v1, v111
	v_cndmask_b32_e32 v122, 0, v30, vcc
	v_lshl_add_u64 v[30:31], v[122:123], 1, s[26:27]
	v_cndmask_b32_e64 v122, 0, v32, s[16:17]
	v_lshl_add_u64 v[32:33], v[122:123], 1, s[26:27]
	v_cndmask_b32_e64 v122, 0, v110, s[18:19]
	s_waitcnt lgkmcnt(1)
	v_add_u32_e32 v112, v112, v1
	s_waitcnt lgkmcnt(0)
	v_cmp_lt_u32_e64 s[12:13], v1, v150
	v_lshl_add_u64 v[110:111], v[122:123], 1, s[26:27]
	v_cmp_lt_u32_e64 s[14:15], v1, v151
	v_cndmask_b32_e64 v122, 0, v112, s[12:13]
	v_lshl_add_u64 v[152:153], v[122:123], 1, s[26:27]
	v_add_u32_e32 v122, v113, v1
	ds_read2_b32 v[112:113], v169 offset0:140 offset1:145
	ds_read2_b32 v[154:155], v170 offset0:140 offset1:145
	v_cndmask_b32_e64 v122, 0, v122, s[14:15]
	v_lshl_add_u64 v[150:151], v[122:123], 1, s[26:27]
	ds_read2_b32 v[176:177], v169 offset0:150 offset1:155
	ds_read2_b32 v[178:179], v170 offset0:150 offset1:155
	s_waitcnt lgkmcnt(3)
	v_add_u32_e32 v112, v112, v1
	s_waitcnt lgkmcnt(2)
	v_cmp_lt_u32_e64 s[10:11], v1, v154
	v_cmp_lt_u32_e64 s[4:5], v1, v155
	s_waitcnt lgkmcnt(0)
	v_cmp_lt_u32_e64 s[6:7], v1, v178
	v_cndmask_b32_e64 v122, 0, v112, s[10:11]
	v_add_u32_e32 v112, v113, v1
	v_lshl_add_u64 v[174:175], v[122:123], 1, s[26:27]
	v_cndmask_b32_e64 v122, 0, v112, s[4:5]
	v_lshl_add_u64 v[112:113], v[122:123], 1, s[26:27]
	global_load_ushort v172, v[124:125], off
	global_load_ushort v161, v[30:31], off
	global_load_ushort v160, v[32:33], off
	global_load_ushort v159, v[110:111], off
	global_load_ushort v157, v[152:153], off
	global_load_ushort v156, v[150:151], off
	global_load_ushort v155, v[174:175], off
	s_nop 0
	global_load_ushort v153, v[112:113], off
	ds_read_b32 v110, v169 offset:640
	ds_read_b32 v111, v170 offset:640
	v_add_u32_e32 v30, v176, v1
	v_cndmask_b32_e64 v122, 0, v30, s[6:7]
	v_add_u32_e32 v32, v177, v1
	v_cmp_lt_u32_e64 s[8:9], v1, v179
	v_lshl_add_u64 v[30:31], v[122:123], 1, s[26:27]
	s_waitcnt lgkmcnt(1)
	v_add_u32_e32 v110, v110, v1
	v_cndmask_b32_e64 v122, 0, v32, s[8:9]
	s_waitcnt lgkmcnt(0)
	v_cmp_lt_u32_e64 s[0:1], v1, v111
	v_lshl_add_u64 v[32:33], v[122:123], 1, s[26:27]
	s_nop 0
	v_cndmask_b32_e64 v122, 0, v110, s[0:1]
	v_lshl_add_u64 v[110:111], v[122:123], 1, s[26:27]
	global_load_ushort v154, v[30:31], off
	global_load_ushort v152, v[32:33], off
	global_load_ushort v151, v[110:111], off
	s_waitcnt vmcnt(42)
	v_cvt_pk_bf16_f32 v30, v134, v135
	v_cvt_pk_bf16_f32 v31, v136, v137
	s_waitcnt vmcnt(41)
	v_cvt_pk_bf16_f32 v32, v130, v131
	v_cvt_pk_bf16_f32 v33, v132, v133
	ds_write2st64_b64 v171, v[30:31], v[32:33] offset1:1
	s_waitcnt vmcnt(40)
	v_cvt_pk_bf16_f32 v30, v102, v103
	v_cvt_pk_bf16_f32 v31, v104, v105
	s_waitcnt vmcnt(39)
	v_cvt_pk_bf16_f32 v32, v90, v91
	v_cvt_pk_bf16_f32 v33, v92, v93
	ds_write2_b64 v171, v[30:31], v[32:33] offset0:130 offset1:194
	s_waitcnt vmcnt(28)
	v_cvt_pk_bf16_f32 v30, v146, v147
	v_cvt_pk_bf16_f32 v31, v148, v149
	v_cvt_pk_bf16_f32 v32, v118, v119
	v_cvt_pk_bf16_f32 v33, v120, v121
	v_add_u32_e32 v90, 32, v171
	ds_write2st64_b64 v90, v[30:31], v[32:33] offset0:4 offset1:5
	v_cvt_pk_bf16_f32 v30, v78, v79
	v_cvt_pk_bf16_f32 v31, v80, v81
	v_cvt_pk_bf16_f32 v32, v126, v127
	v_cvt_pk_bf16_f32 v33, v128, v129
	v_add_u32_e32 v78, 48, v171
	ds_write2st64_b64 v78, v[30:31], v[32:33] offset0:6 offset1:7
	v_cvt_pk_bf16_f32 v30, v74, v75
	v_cvt_pk_bf16_f32 v31, v76, v77
	v_cvt_pk_bf16_f32 v32, v62, v63
	v_cvt_pk_bf16_f32 v33, v64, v65
	v_add_u32_e32 v62, 64, v171
	ds_write2st64_b64 v62, v[30:31], v[32:33] offset0:8 offset1:9
	v_cvt_pk_bf16_f32 v30, v58, v59
	v_cvt_pk_bf16_f32 v31, v60, v61
	v_cvt_pk_bf16_f32 v32, v46, v47
	v_cvt_pk_bf16_f32 v33, v48, v49
	v_add_u32_e32 v46, 0x50, v171
	ds_write2st64_b64 v46, v[30:31], v[32:33] offset0:10 offset1:11
	v_cvt_pk_bf16_f32 v30, v54, v55
	v_cvt_pk_bf16_f32 v31, v56, v57
	v_cvt_pk_bf16_f32 v32, v42, v43
	v_cvt_pk_bf16_f32 v33, v44, v45
	v_add_u32_e32 v42, 0x60, v171
	v_cvt_pk_bf16_f32 v22, v22, v23
	v_cvt_pk_bf16_f32 v23, v24, v25
	s_waitcnt vmcnt(27)
	v_cvt_pk_bf16_f32 v18, v18, v19
	v_cvt_pk_bf16_f32 v19, v20, v21
	v_add_u32_e32 v20, 0x70, v171
	ds_write2st64_b64 v42, v[30:31], v[32:33] offset0:12 offset1:13
	ds_write2st64_b64 v20, v[22:23], v[18:19] offset0:14 offset1:15
	v_mov_b32_e32 v18, 0xa0
	v_lshl_add_u32 v150, v164, 4, v18
	v_add_u32_e32 v18, s33, v150
	v_min_i32_e32 v18, 0x18698, v18
	v_ashrrev_i32_e32 v19, 31, v18
	v_lshlrev_b64 v[18:19], 11, v[18:19]
	v_lshl_add_u64 v[18:19], v[162:163], 0, v[18:19]
	v_add_co_u32_e64 v20, s[22:23], s34, v18
	global_load_dwordx4 v[134:137], v[18:19], off nt
	global_load_dwordx4 v[126:129], v[18:19], off offset:1024 nt
	global_load_dwordx4 v[110:113], v[18:19], off offset:2048 nt
	global_load_dwordx4 v[102:105], v[18:19], off offset:3072 nt
	v_addc_co_u32_e64 v21, s[22:23], 0, v19, s[22:23]
	v_add_co_u32_e64 v22, s[22:23], s35, v18
	s_nop 1
	v_addc_co_u32_e64 v23, s[22:23], 0, v19, s[22:23]
	v_add_co_u32_e64 v18, s[22:23], s36, v18
	global_load_dwordx4 v[118:121], v[20:21], off offset:1024 nt
	global_load_dwordx4 v[90:93], v[20:21], off offset:2048 nt
	global_load_dwordx4 v[78:81], v[22:23], off nt
	global_load_dwordx4 v[74:77], v[22:23], off offset:1024 nt
	global_load_dwordx4 v[62:65], v[22:23], off offset:2048 nt
	global_load_dwordx4 v[54:57], v[22:23], off offset:3072 nt
	v_addc_co_u32_e64 v19, s[22:23], 0, v19, s[22:23]
	global_load_dwordx4 v[122:125], v[20:21], off offset:3072 nt
	global_load_dwordx4 v[58:61], v[18:19], off nt
	global_load_dwordx4 v[46:49], v[18:19], off offset:1024 nt
	global_load_dwordx4 v[30:33], v[18:19], off offset:2048 nt
	global_load_dwordx4 v[146:149], v[22:23], off offset:-4096 nt
	s_nop 0
	global_load_dwordx4 v[22:25], v[18:19], off offset:3072 nt
	s_waitcnt vmcnt(42)
	v_cvt_pk_bf16_f32 v18, v138, v139
	v_cvt_pk_bf16_f32 v19, v140, v141
	s_waitcnt vmcnt(41)
	v_cvt_pk_bf16_f32 v20, v114, v115
	v_cvt_pk_bf16_f32 v21, v116, v117
	v_add_u32_e32 v42, 0x80, v171
	ds_write2st64_b64 v42, v[18:19], v[20:21] offset0:16 offset1:17
	s_waitcnt vmcnt(40)
	v_cvt_pk_bf16_f32 v18, v106, v107
	v_cvt_pk_bf16_f32 v19, v108, v109
	s_waitcnt vmcnt(39)
	v_cvt_pk_bf16_f32 v20, v94, v95
	v_cvt_pk_bf16_f32 v21, v96, v97
	v_add_u32_e32 v42, 0x90, v171
	ds_write2st64_b64 v42, v[18:19], v[20:21] offset0:18 offset1:19
	s_waitcnt vmcnt(28)
	v_cvt_pk_bf16_f32 v18, v142, v143
	v_cvt_pk_bf16_f32 v19, v144, v145
	v_cvt_pk_bf16_f32 v20, v98, v99
	v_cvt_pk_bf16_f32 v21, v100, v101
	v_add_u32_e32 v42, 0xa0, v171
	ds_write2st64_b64 v42, v[18:19], v[20:21] offset0:20 offset1:21
	v_cvt_pk_bf16_f32 v18, v82, v83
	v_cvt_pk_bf16_f32 v19, v84, v85
	v_cvt_pk_bf16_f32 v20, v86, v87
	v_cvt_pk_bf16_f32 v21, v88, v89
	v_add_u32_e32 v42, 0xb0, v171
	ds_write2st64_b64 v42, v[18:19], v[20:21] offset0:22 offset1:23
	v_cvt_pk_bf16_f32 v18, v70, v71
	v_cvt_pk_bf16_f32 v19, v72, v73
	v_cvt_pk_bf16_f32 v20, v66, v67
	v_cvt_pk_bf16_f32 v21, v68, v69
	v_add_u32_e32 v42, 0xc0, v171
	ds_write2st64_b64 v42, v[18:19], v[20:21] offset0:24 offset1:25
	v_cvt_pk_bf16_f32 v18, v50, v51
	v_cvt_pk_bf16_f32 v19, v52, v53
	v_cvt_pk_bf16_f32 v20, v34, v35
	v_cvt_pk_bf16_f32 v21, v36, v37
	v_add_u32_e32 v34, 0xd0, v171
	ds_write2st64_b64 v34, v[18:19], v[20:21] offset0:26 offset1:27
	v_cvt_pk_bf16_f32 v18, v38, v39
	v_cvt_pk_bf16_f32 v19, v40, v41
	v_cvt_pk_bf16_f32 v20, v26, v27
	v_cvt_pk_bf16_f32 v21, v28, v29
	v_add_u32_e32 v26, 0xe0, v171
	v_cvt_pk_bf16_f32 v14, v14, v15
	v_cvt_pk_bf16_f32 v15, v16, v17
	s_waitcnt vmcnt(27)
	v_cvt_pk_bf16_f32 v10, v10, v11
	v_cvt_pk_bf16_f32 v11, v12, v13
	v_add_u32_e32 v12, 0xf0, v171
	ds_write2st64_b64 v26, v[18:19], v[20:21] offset0:28 offset1:29
	ds_write2st64_b64 v12, v[14:15], v[10:11] offset0:30 offset1:31
	v_add_u32_e32 v10, s31, v150
	v_min_i32_e32 v10, 0x18698, v10
	v_ashrrev_i32_e32 v11, 31, v10
	v_lshlrev_b64 v[10:11], 11, v[10:11]
	v_lshl_add_u64 v[10:11], v[162:163], 0, v[10:11]
	v_add_co_u32_e64 v12, s[22:23], s34, v10
	global_load_dwordx4 v[138:141], v[10:11], off nt
	global_load_dwordx4 v[130:133], v[10:11], off offset:1024 nt
	global_load_dwordx4 v[114:117], v[10:11], off offset:2048 nt
	global_load_dwordx4 v[94:97], v[10:11], off offset:3072 nt
	v_addc_co_u32_e64 v13, s[22:23], 0, v11, s[22:23]
	v_add_co_u32_e64 v14, s[22:23], s35, v10
	s_nop 1
	v_addc_co_u32_e64 v15, s[22:23], 0, v11, s[22:23]
	v_add_co_u32_e64 v10, s[22:23], s36, v10
	global_load_dwordx4 v[98:101], v[12:13], off offset:1024 nt
	global_load_dwordx4 v[82:85], v[12:13], off offset:2048 nt
	global_load_dwordx4 v[70:73], v[14:15], off nt
	global_load_dwordx4 v[66:69], v[14:15], off offset:1024 nt
	global_load_dwordx4 v[50:53], v[14:15], off offset:2048 nt
	global_load_dwordx4 v[38:41], v[14:15], off offset:3072 nt
	v_addc_co_u32_e64 v11, s[22:23], 0, v11, s[22:23]
	global_load_dwordx4 v[86:89], v[12:13], off offset:3072 nt
	global_load_dwordx4 v[42:45], v[10:11], off nt
	global_load_dwordx4 v[34:37], v[10:11], off offset:1024 nt
	global_load_dwordx4 v[18:21], v[10:11], off offset:2048 nt
	global_load_dwordx4 v[142:145], v[14:15], off offset:-4096 nt
	s_nop 0
	global_load_dwordx4 v[14:17], v[10:11], off offset:3072 nt
	v_mov_b32_e32 v10, 0x14500
	v_lshl_add_u32 v173, v173, 4, v10
	ds_read_b128 v[10:13], v173
	ds_read_b128 v[26:29], v173 offset:1024
	ds_read_b128 v[106:109], v168
	ds_read_b128 v[174:177], v168 offset:16
	s_waitcnt lgkmcnt(1)
	v_mfma_f32_16x16x32_bf16 v[10:13], v[10:13], v[106:109], 0
	ds_read_b128 v[106:109], v173 offset:2048
	ds_read_b128 v[178:181], v173 offset:3072
	s_waitcnt lgkmcnt(2)
	v_mfma_f32_16x16x32_bf16 v[10:13], v[26:29], v[174:177], v[10:13]
	ds_read_b128 v[26:29], v168 offset:32
	ds_read_b128 v[174:177], v168 offset:48
	s_waitcnt lgkmcnt(1)
	v_mfma_f32_16x16x32_bf16 v[10:13], v[106:109], v[26:29], v[10:13]
	s_waitcnt lgkmcnt(0)
	v_mfma_f32_16x16x32_bf16 v[10:13], v[178:181], v[174:177], v[10:13]
	ds_read_b128 v[26:29], v173 offset:4096
	ds_read_b128 v[106:109], v173 offset:5120
	ds_read_b128 v[174:177], v168 offset:64
	ds_read_b128 v[178:181], v168 offset:80
	s_waitcnt lgkmcnt(1)
	v_mfma_f32_16x16x32_bf16 v[10:13], v[26:29], v[174:177], v[10:13]
	ds_read_b128 v[26:29], v173 offset:6144
	ds_read_b128 v[174:177], v173 offset:7168
	s_waitcnt lgkmcnt(2)
	v_mfma_f32_16x16x32_bf16 v[10:13], v[106:109], v[178:181], v[10:13]
	ds_read_b128 v[106:109], v168 offset:96
	ds_read_b128 v[178:181], v168 offset:112
	s_waitcnt lgkmcnt(1)
	v_mfma_f32_16x16x32_bf16 v[10:13], v[26:29], v[106:109], v[10:13]
	s_waitcnt lgkmcnt(0)
	v_mfma_f32_16x16x32_bf16 v[10:13], v[174:177], v[178:181], v[10:13]
	ds_read_b128 v[26:29], v173 offset:8192
	ds_read_b128 v[106:109], v173 offset:9216
	ds_read_b128 v[174:177], v168 offset:128
	ds_read_b128 v[178:181], v168 offset:144
	s_waitcnt lgkmcnt(1)
	v_mfma_f32_16x16x32_bf16 v[10:13], v[26:29], v[174:177], v[10:13]
	ds_read_b128 v[26:29], v173 offset:10240
	ds_read_b128 v[174:177], v173 offset:11264
	s_waitcnt lgkmcnt(2)
	v_mfma_f32_16x16x32_bf16 v[10:13], v[106:109], v[178:181], v[10:13]
	ds_read_b128 v[106:109], v168 offset:160
	ds_read_b128 v[178:181], v168 offset:176
	s_waitcnt lgkmcnt(1)
	v_mfma_f32_16x16x32_bf16 v[10:13], v[26:29], v[106:109], v[10:13]
	s_waitcnt lgkmcnt(0)
	v_mfma_f32_16x16x32_bf16 v[10:13], v[174:177], v[178:181], v[10:13]
	ds_read_b128 v[26:29], v173 offset:12288
	ds_read_b128 v[106:109], v173 offset:13312
	ds_read_b128 v[174:177], v168 offset:192
	ds_read_b128 v[178:181], v168 offset:208
	s_waitcnt lgkmcnt(1)
	v_mfma_f32_16x16x32_bf16 v[10:13], v[26:29], v[174:177], v[10:13]
	ds_read_b128 v[26:29], v173 offset:14336
	ds_read_b128 v[174:177], v173 offset:15360
	s_waitcnt lgkmcnt(2)
	v_mfma_f32_16x16x32_bf16 v[10:13], v[106:109], v[178:181], v[10:13]
	ds_read_b128 v[106:109], v168 offset:224
	ds_read_b128 v[178:181], v168 offset:240
	s_waitcnt lgkmcnt(1)
	v_mfma_f32_16x16x32_bf16 v[10:13], v[26:29], v[106:109], v[10:13]
	s_waitcnt lgkmcnt(0)
	v_mfma_f32_16x16x32_bf16 v[10:13], v[174:177], v[178:181], v[10:13]
	s_waitcnt vmcnt(42)
	v_cmp_ne_u16_e64 s[22:23], -1, v172
	s_and_b64 s[22:23], s[20:21], s[22:23]
	s_and_saveexec_b64 s[20:21], s[22:23]
	v_and_b32_e32 v26, 0xffff, v172
	v_mov_b32_e32 v27, 0x18500
	v_lshl_add_u32 v26, v26, 2, v27
	v_mov_b32_e32 v27, 1
	ds_add_u32 v26, v27
	s_or_b64 exec, exec, s[20:21]
	v_mov_b32_e32 v26, 0xffff
	s_mov_b32 s22, 0xffff
	s_waitcnt vmcnt(41)
	v_cndmask_b32_sdwa v27, v26, v161, vcc dst_sel:DWORD dst_unused:UNUSED_PAD src0_sel:DWORD src1_sel:WORD_0
	v_cmp_ne_u32_e32 vcc, s22, v27
	s_and_saveexec_b64 s[20:21], vcc
	v_mov_b32_e32 v28, 0x18500
	v_lshl_add_u32 v27, v27, 2, v28
	v_mov_b32_e32 v28, 1
	ds_add_u32 v27, v28
	s_or_b64 exec, exec, s[20:21]
	s_mov_b64 vcc, s[16:17]
	s_waitcnt vmcnt(40)
	v_cndmask_b32_sdwa v26, v26, v160, vcc dst_sel:DWORD dst_unused:UNUSED_PAD src0_sel:DWORD src1_sel:WORD_0
	v_cmp_ne_u32_e32 vcc, s22, v26
	s_and_saveexec_b64 s[16:17], vcc
	v_mov_b32_e32 v27, 0x18500
	v_lshl_add_u32 v26, v26, 2, v27
	v_mov_b32_e32 v27, 1
	ds_add_u32 v26, v27
	s_or_b64 exec, exec, s[16:17]
	s_mov_b64 vcc, s[18:19]
	v_mov_b32_e32 v26, 0xffff
	s_mov_b32 s18, 0xffff
	s_waitcnt vmcnt(39)
	v_cndmask_b32_sdwa v27, v26, v159, vcc dst_sel:DWORD dst_unused:UNUSED_PAD src0_sel:DWORD src1_sel:WORD_0
	v_cmp_ne_u32_e32 vcc, s18, v27
	s_and_saveexec_b64 s[16:17], vcc
	v_mov_b32_e32 v28, 0x18500
	v_lshl_add_u32 v27, v27, 2, v28
	v_mov_b32_e32 v28, 1
	ds_add_u32 v27, v28
	s_or_b64 exec, exec, s[16:17]
	s_mov_b64 vcc, s[12:13]
	s_waitcnt vmcnt(38)
	v_cndmask_b32_sdwa v26, v26, v157, vcc dst_sel:DWORD dst_unused:UNUSED_PAD src0_sel:DWORD src1_sel:WORD_0
	v_cmp_ne_u32_e32 vcc, s18, v26
	s_and_saveexec_b64 s[12:13], vcc
	v_mov_b32_e32 v27, 0x18500
	v_lshl_add_u32 v26, v26, 2, v27
	v_mov_b32_e32 v27, 1
	ds_add_u32 v26, v27
	s_or_b64 exec, exec, s[12:13]
	s_mov_b64 vcc, s[14:15]
	v_mov_b32_e32 v26, 0xffff
	s_mov_b32 s14, 0xffff
	s_waitcnt vmcnt(37)
	v_cndmask_b32_sdwa v27, v26, v156, vcc dst_sel:DWORD dst_unused:UNUSED_PAD src0_sel:DWORD src1_sel:WORD_0
	v_cmp_ne_u32_e32 vcc, s14, v27
	s_and_saveexec_b64 s[12:13], vcc
	v_mov_b32_e32 v28, 0x18500
	v_lshl_add_u32 v27, v27, 2, v28
	v_mov_b32_e32 v28, 1
	ds_add_u32 v27, v28
	s_or_b64 exec, exec, s[12:13]
	s_mov_b64 vcc, s[10:11]
	s_waitcnt vmcnt(36)
	v_cndmask_b32_sdwa v26, v26, v155, vcc dst_sel:DWORD dst_unused:UNUSED_PAD src0_sel:DWORD src1_sel:WORD_0
	v_cmp_ne_u32_e32 vcc, s14, v26
	s_and_saveexec_b64 s[10:11], vcc
	v_mov_b32_e32 v27, 0x18500
	v_lshl_add_u32 v26, v26, 2, v27
	v_mov_b32_e32 v27, 1
	ds_add_u32 v26, v27
	s_or_b64 exec, exec, s[10:11]
	s_mov_b64 vcc, s[4:5]
	v_mov_b32_e32 v26, 0xffff
	s_mov_b32 s10, 0xffff
	s_waitcnt vmcnt(35)
	v_cndmask_b32_sdwa v27, v26, v153, vcc dst_sel:DWORD dst_unused:UNUSED_PAD src0_sel:DWORD src1_sel:WORD_0
	v_cmp_ne_u32_e32 vcc, s10, v27
	s_and_saveexec_b64 s[4:5], vcc
	v_mov_b32_e32 v28, 0x18500
	v_lshl_add_u32 v27, v27, 2, v28
	v_mov_b32_e32 v28, 1
	ds_add_u32 v27, v28
	s_or_b64 exec, exec, s[4:5]
	s_mov_b64 vcc, s[6:7]
	s_waitcnt vmcnt(34)
	v_cndmask_b32_sdwa v26, v26, v154, vcc dst_sel:DWORD dst_unused:UNUSED_PAD src0_sel:DWORD src1_sel:WORD_0
	v_cmp_ne_u32_e32 vcc, s10, v26
	s_and_saveexec_b64 s[4:5], vcc
	v_mov_b32_e32 v27, 0x18500
	v_lshl_add_u32 v26, v26, 2, v27
	v_mov_b32_e32 v27, 1
	ds_add_u32 v26, v27
	s_or_b64 exec, exec, s[4:5]
	s_mov_b64 vcc, s[8:9]
	v_mov_b32_e32 v26, 0xffff
	s_mov_b32 s6, 0xffff
	s_waitcnt vmcnt(33)
	v_cndmask_b32_sdwa v27, v26, v152, vcc dst_sel:DWORD dst_unused:UNUSED_PAD src0_sel:DWORD src1_sel:WORD_0
	v_cmp_ne_u32_e32 vcc, s6, v27
	s_and_saveexec_b64 s[4:5], vcc
	v_mov_b32_e32 v28, 0x18500
	v_lshl_add_u32 v27, v27, 2, v28
	v_mov_b32_e32 v28, 1
	ds_add_u32 v27, v28
	s_or_b64 exec, exec, s[4:5]
	s_mov_b64 vcc, s[0:1]
	s_waitcnt vmcnt(32)
	v_cndmask_b32_sdwa v26, v26, v151, vcc dst_sel:DWORD dst_unused:UNUSED_PAD src0_sel:DWORD src1_sel:WORD_0
	v_cmp_ne_u32_e32 vcc, s6, v26
	s_and_saveexec_b64 s[0:1], vcc
	v_mov_b32_e32 v27, 0x18500
	v_lshl_add_u32 v26, v26, 2, v27
	v_mov_b32_e32 v27, 1
	ds_add_u32 v26, v27
	s_or_b64 exec, exec, s[0:1]
	v_mov_b32_e32 v173, v1
	ds_read2_b32 v[26:27], v169 offset0:165 offset1:170
	ds_read2_b32 v[28:29], v170 offset0:165 offset1:170
	ds_read2_b32 v[106:107], v170 offset0:175 offset1:180
	ds_read2_b32 v[108:109], v169 offset0:175 offset1:180
	v_mov_b32_e32 v175, 0
	s_waitcnt lgkmcnt(3)
	v_add_u32_e32 v26, v26, v1
	s_waitcnt lgkmcnt(2)
	v_cmp_lt_u32_e64 s[20:21], v1, v28
	s_waitcnt lgkmcnt(1)
	v_cmp_lt_u32_e64 s[16:17], v1, v106
	s_waitcnt lgkmcnt(0)
	v_add_u32_e32 v28, v108, v1
	v_add_u32_e32 v106, v109, v1
	ds_read2_b32 v[108:109], v169 offset0:185 offset1:190
	ds_read2_b32 v[154:155], v170 offset0:185 offset1:190
	v_cndmask_b32_e64 v174, 0, v26, s[20:21]
	v_add_u32_e32 v26, v27, v1
	v_cmp_lt_u32_e32 vcc, v1, v29
	v_lshl_add_u64 v[152:153], v[174:175], 1, s[26:27]
	v_cmp_lt_u32_e64 s[18:19], v1, v107
	v_cndmask_b32_e32 v174, 0, v26, vcc
	v_lshl_add_u64 v[26:27], v[174:175], 1, s[26:27]
	v_cndmask_b32_e64 v174, 0, v28, s[16:17]
	v_lshl_add_u64 v[28:29], v[174:175], 1, s[26:27]
	v_cndmask_b32_e64 v174, 0, v106, s[18:19]
	s_waitcnt lgkmcnt(1)
	v_add_u32_e32 v108, v108, v1
	s_waitcnt lgkmcnt(0)
	v_cmp_lt_u32_e64 s[12:13], v1, v154
	v_lshl_add_u64 v[106:107], v[174:175], 1, s[26:27]
	v_add_u32_e32 v151, v109, v1
	v_cndmask_b32_e64 v174, 0, v108, s[12:13]
	ds_read2_b32 v[108:109], v169 offset0:195 offset1:200
	ds_read2_b32 v[160:161], v170 offset0:195 offset1:200
	v_cmp_lt_u32_e64 s[14:15], v1, v155
	v_lshl_add_u64 v[156:157], v[174:175], 1, s[26:27]
	ds_read2_b32 v[178:179], v169 offset0:205 offset1:210
	ds_read2_b32 v[180:181], v170 offset0:205 offset1:210
	v_cndmask_b32_e64 v174, 0, v151, s[14:15]
	s_waitcnt lgkmcnt(3)
	v_add_u32_e32 v108, v108, v1
	s_waitcnt lgkmcnt(2)
	v_cmp_lt_u32_e64 s[10:11], v1, v160
	v_lshl_add_u64 v[154:155], v[174:175], 1, s[26:27]
	v_cmp_lt_u32_e64 s[4:5], v1, v161
	v_cndmask_b32_e64 v174, 0, v108, s[10:11]
	v_add_u32_e32 v108, v109, v1
	v_lshl_add_u64 v[176:177], v[174:175], 1, s[26:27]
	v_cndmask_b32_e64 v174, 0, v108, s[4:5]
	v_lshl_add_u64 v[108:109], v[174:175], 1, s[26:27]
	global_load_ushort v172, v[152:153], off
	global_load_ushort v161, v[26:27], off
	global_load_ushort v160, v[28:29], off
	global_load_ushort v159, v[106:107], off
	s_nop 0
	global_load_ushort v157, v[156:157], off
	s_nop 0
	global_load_ushort v156, v[154:155], off
	s_nop 0
	global_load_ushort v155, v[176:177], off
	global_load_ushort v153, v[108:109], off
	ds_read_b32 v106, v169 offset:860
	ds_read_b32 v107, v170 offset:860
	s_waitcnt lgkmcnt(3)
	v_add_u32_e32 v26, v178, v1
	s_waitcnt lgkmcnt(2)
	v_cmp_lt_u32_e64 s[6:7], v1, v180
	v_add_u32_e32 v28, v179, v1
	v_cmp_lt_u32_e64 s[8:9], v1, v181
	v_cndmask_b32_e64 v174, 0, v26, s[6:7]
	v_lshl_add_u64 v[26:27], v[174:175], 1, s[26:27]
	v_cndmask_b32_e64 v174, 0, v28, s[8:9]
	s_waitcnt lgkmcnt(1)
	v_add_u32_e32 v106, v106, v1
	s_waitcnt lgkmcnt(0)
	v_cmp_lt_u32_e64 s[0:1], v1, v107
	v_lshl_add_u64 v[28:29], v[174:175], 1, s[26:27]
	s_nop 0
	v_cndmask_b32_e64 v174, 0, v106, s[0:1]
	v_lshl_add_u64 v[106:107], v[174:175], 1, s[26:27]
	global_load_ushort v154, v[26:27], off
	global_load_ushort v152, v[28:29], off
	global_load_ushort v151, v[106:107], off
	s_waitcnt vmcnt(42)
	v_cvt_pk_bf16_f32 v26, v134, v135
	v_cvt_pk_bf16_f32 v27, v136, v137
	s_waitcnt vmcnt(41)
	v_cvt_pk_bf16_f32 v28, v126, v127
	v_cvt_pk_bf16_f32 v29, v128, v129
	ds_write2st64_b64 v171, v[26:27], v[28:29] offset1:1
	s_waitcnt vmcnt(40)
	v_cvt_pk_bf16_f32 v26, v110, v111
	v_cvt_pk_bf16_f32 v27, v112, v113
	s_waitcnt vmcnt(39)
	v_cvt_pk_bf16_f32 v28, v102, v103
	v_cvt_pk_bf16_f32 v29, v104, v105
	ds_write2_b64 v171, v[26:27], v[28:29] offset0:130 offset1:194
	s_waitcnt vmcnt(28)
	v_cvt_pk_bf16_f32 v26, v146, v147
	v_cvt_pk_bf16_f32 v27, v148, v149
	v_cvt_pk_bf16_f32 v28, v118, v119
	v_cvt_pk_bf16_f32 v29, v120, v121
	v_add_u32_e32 v102, 32, v171
	ds_write2st64_b64 v102, v[26:27], v[28:29] offset0:4 offset1:5
	v_cvt_pk_bf16_f32 v26, v90, v91
	v_cvt_pk_bf16_f32 v27, v92, v93
	v_cvt_pk_bf16_f32 v28, v122, v123
	v_cvt_pk_bf16_f32 v29, v124, v125
	v_add_u32_e32 v90, 48, v171
	ds_write2st64_b64 v90, v[26:27], v[28:29] offset0:6 offset1:7
	v_cvt_pk_bf16_f32 v26, v78, v79
	v_cvt_pk_bf16_f32 v27, v80, v81
	v_cvt_pk_bf16_f32 v28, v74, v75
	v_cvt_pk_bf16_f32 v29, v76, v77
	v_add_u32_e32 v74, 64, v171
	ds_write2st64_b64 v74, v[26:27], v[28:29] offset0:8 offset1:9
	v_cvt_pk_bf16_f32 v26, v62, v63
	v_cvt_pk_bf16_f32 v27, v64, v65
	v_cvt_pk_bf16_f32 v28, v54, v55
	v_cvt_pk_bf16_f32 v29, v56, v57
	v_add_u32_e32 v54, 0x50, v171
	ds_write2st64_b64 v54, v[26:27], v[28:29] offset0:10 offset1:11
	v_cvt_pk_bf16_f32 v26, v58, v59
	v_cvt_pk_bf16_f32 v27, v60, v61
	v_cvt_pk_bf16_f32 v28, v46, v47
	v_cvt_pk_bf16_f32 v29, v48, v49
	v_add_u32_e32 v46, 0x60, v171
	ds_write2st64_b64 v46, v[26:27], v[28:29] offset0:12 offset1:13
	v_cvt_pk_bf16_f32 v26, v30, v31
	v_cvt_pk_bf16_f32 v27, v32, v33
	s_waitcnt vmcnt(27)
	v_cvt_pk_bf16_f32 v22, v22, v23
	v_cvt_pk_bf16_f32 v23, v24, v25
	v_add_u32_e32 v24, 0x70, v171
	ds_write2st64_b64 v24, v[26:27], v[22:23] offset0:14 offset1:15
	v_mov_b32_e32 v22, 0xf0
	v_lshl_add_u32 v146, v164, 4, v22
	v_add_u32_e32 v22, s33, v146
	v_min_i32_e32 v22, 0x18698, v22
	v_ashrrev_i32_e32 v23, 31, v22
	v_lshlrev_b64 v[22:23], 11, v[22:23]
	v_lshl_add_u64 v[22:23], v[162:163], 0, v[22:23]
	s_movk_i32 s33, 0x1000
	v_add_co_u32_e64 v24, s[22:23], s33, v22
	s_movk_i32 s34, 0x2000
	s_nop 0
	v_addc_co_u32_e64 v25, s[22:23], 0, v23, s[22:23]
	v_add_co_u32_e64 v126, s[22:23], s34, v22
	s_movk_i32 s35, 0x3000
	s_nop 0
	v_addc_co_u32_e64 v127, s[22:23], 0, v23, s[22:23]
	global_load_dwordx4 v[122:125], v[22:23], off nt
	global_load_dwordx4 v[118:121], v[22:23], off offset:1024 nt
	global_load_dwordx4 v[102:105], v[22:23], off offset:2048 nt
	global_load_dwordx4 v[90:93], v[22:23], off offset:3072 nt
	v_add_co_u32_e64 v22, s[22:23], s35, v22
	global_load_dwordx4 v[106:109], v[24:25], off offset:1024 nt
	global_load_dwordx4 v[78:81], v[24:25], off offset:2048 nt
	global_load_dwordx4 v[74:77], v[126:127], off nt
	global_load_dwordx4 v[62:65], v[126:127], off offset:1024 nt
	global_load_dwordx4 v[58:61], v[126:127], off offset:2048 nt
	global_load_dwordx4 v[46:49], v[126:127], off offset:3072 nt
	v_addc_co_u32_e64 v23, s[22:23], 0, v23, s[22:23]
	global_load_dwordx4 v[110:113], v[24:25], off offset:3072 nt
	global_load_dwordx4 v[54:57], v[22:23], off nt
	global_load_dwordx4 v[30:33], v[22:23], off offset:1024 nt
	global_load_dwordx4 v[26:29], v[22:23], off offset:2048 nt
	s_nop 0
	global_load_dwordx4 v[126:129], v[126:127], off offset:-4096 nt
	s_nop 0
	global_load_dwordx4 v[22:25], v[22:23], off offset:3072 nt
	s_waitcnt vmcnt(40)
	v_cvt_pk_bf16_f32 v114, v114, v115
	v_cvt_pk_bf16_f32 v115, v116, v117
	s_waitcnt vmcnt(39)
	v_cvt_pk_bf16_f32 v94, v94, v95
	v_cvt_pk_bf16_f32 v95, v96, v97
	v_add_u32_e32 v96, 0x90, v171
	s_waitcnt vmcnt(34)
	v_cvt_pk_bf16_f32 v50, v50, v51
	v_cvt_pk_bf16_f32 v51, v52, v53
	s_waitcnt vmcnt(33)
	v_cvt_pk_bf16_f32 v38, v38, v39
	v_cvt_pk_bf16_f32 v39, v40, v41
	v_add_u32_e32 v40, 0xd0, v171
	v_cvt_pk_bf16_f32 v134, v138, v139
	v_cvt_pk_bf16_f32 v135, v140, v141
	v_cvt_pk_bf16_f32 v130, v130, v131
	v_cvt_pk_bf16_f32 v131, v132, v133
	v_add_u32_e32 v132, 0x80, v171
	ds_write2st64_b64 v96, v[114:115], v[94:95] offset0:18 offset1:19
	s_waitcnt vmcnt(28)
	v_cvt_pk_bf16_f32 v94, v142, v143
	v_cvt_pk_bf16_f32 v95, v144, v145
	v_cvt_pk_bf16_f32 v96, v98, v99
	v_cvt_pk_bf16_f32 v97, v100, v101
	v_add_u32_e32 v98, 0xa0, v171
	v_cvt_pk_bf16_f32 v82, v82, v83
	v_cvt_pk_bf16_f32 v83, v84, v85
	v_cvt_pk_bf16_f32 v84, v86, v87
	v_cvt_pk_bf16_f32 v85, v88, v89
	v_add_u32_e32 v86, 0xb0, v171
	v_cvt_pk_bf16_f32 v70, v70, v71
	v_cvt_pk_bf16_f32 v71, v72, v73
	v_cvt_pk_bf16_f32 v66, v66, v67
	v_cvt_pk_bf16_f32 v67, v68, v69
	v_add_u32_e32 v68, 0xc0, v171
	ds_write2st64_b64 v40, v[50:51], v[38:39] offset0:26 offset1:27
	v_cvt_pk_bf16_f32 v38, v42, v43
	v_cvt_pk_bf16_f32 v39, v44, v45
	v_cvt_pk_bf16_f32 v34, v34, v35
	v_cvt_pk_bf16_f32 v35, v36, v37
	v_add_u32_e32 v36, 0xe0, v171
	v_cvt_pk_bf16_f32 v18, v18, v19
	v_cvt_pk_bf16_f32 v19, v20, v21
	s_waitcnt vmcnt(27)
	v_cvt_pk_bf16_f32 v14, v14, v15
	v_cvt_pk_bf16_f32 v15, v16, v17
	v_add_u32_e32 v16, 0xf0, v171
	ds_write2st64_b64 v132, v[134:135], v[130:131] offset0:16 offset1:17
	ds_write2st64_b64 v98, v[94:95], v[96:97] offset0:20 offset1:21
	ds_write2st64_b64 v86, v[82:83], v[84:85] offset0:22 offset1:23
	ds_write2st64_b64 v68, v[70:71], v[66:67] offset0:24 offset1:25
	ds_write2st64_b64 v36, v[38:39], v[34:35] offset0:28 offset1:29
	ds_write2st64_b64 v16, v[18:19], v[14:15] offset0:30 offset1:31
	v_add_u32_e32 v14, s31, v146
	v_min_i32_e32 v14, 0x18698, v14
	v_ashrrev_i32_e32 v15, 31, v14
	v_lshlrev_b64 v[14:15], 11, v[14:15]
	v_lshl_add_u64 v[14:15], v[162:163], 0, v[14:15]
	v_add_co_u32_e64 v16, s[22:23], s33, v14
	global_load_dwordx4 v[138:141], v[14:15], off nt
	global_load_dwordx4 v[134:137], v[14:15], off offset:1024 nt
	global_load_dwordx4 v[130:133], v[14:15], off offset:2048 nt
	global_load_dwordx4 v[98:101], v[14:15], off offset:3072 nt
	v_addc_co_u32_e64 v17, s[22:23], 0, v15, s[22:23]
	v_add_co_u32_e64 v18, s[22:23], s34, v14
	s_nop 1
	v_addc_co_u32_e64 v19, s[22:23], 0, v15, s[22:23]
	v_add_co_u32_e64 v14, s[22:23], s35, v14
	global_load_dwordx4 v[114:117], v[16:17], off offset:1024 nt
	global_load_dwordx4 v[86:89], v[16:17], off offset:2048 nt
	global_load_dwordx4 v[82:85], v[18:19], off nt
	global_load_dwordx4 v[70:73], v[18:19], off offset:1024 nt
	global_load_dwordx4 v[66:69], v[18:19], off offset:2048 nt
	global_load_dwordx4 v[42:45], v[18:19], off offset:3072 nt
	v_addc_co_u32_e64 v15, s[22:23], 0, v15, s[22:23]
	global_load_dwordx4 v[94:97], v[16:17], off offset:3072 nt
	global_load_dwordx4 v[50:53], v[14:15], off nt
	global_load_dwordx4 v[38:41], v[14:15], off offset:1024 nt
	global_load_dwordx4 v[34:37], v[14:15], off offset:2048 nt
	global_load_dwordx4 v[142:145], v[18:19], off offset:-4096 nt
	s_nop 0
	global_load_dwordx4 v[18:21], v[14:15], off offset:3072 nt
	v_mov_b32_e32 v14, 0x14500
	v_lshl_add_u32 v147, v173, 4, v14
	ds_read_b128 v[14:17], v147
	ds_read_b128 v[174:177], v147 offset:1024
	ds_read_b128 v[178:181], v168
	ds_read_b128 v[182:185], v168 offset:16
	s_waitcnt lgkmcnt(1)
	v_mfma_f32_16x16x32_bf16 v[14:17], v[14:17], v[178:181], 0
	ds_read_b128 v[178:181], v147 offset:2048
	ds_read_b128 v[186:189], v147 offset:3072
	s_waitcnt lgkmcnt(2)
	v_mfma_f32_16x16x32_bf16 v[14:17], v[174:177], v[182:185], v[14:17]
	ds_read_b128 v[174:177], v168 offset:32
	ds_read_b128 v[182:185], v168 offset:48
	s_waitcnt lgkmcnt(1)
	v_mfma_f32_16x16x32_bf16 v[14:17], v[178:181], v[174:177], v[14:17]
	s_waitcnt lgkmcnt(0)
	v_mfma_f32_16x16x32_bf16 v[14:17], v[186:189], v[182:185], v[14:17]
	ds_read_b128 v[174:177], v147 offset:4096
	ds_read_b128 v[178:181], v147 offset:5120
	ds_read_b128 v[182:185], v168 offset:64
	ds_read_b128 v[186:189], v168 offset:80
	s_waitcnt lgkmcnt(1)
	v_mfma_f32_16x16x32_bf16 v[14:17], v[174:177], v[182:185], v[14:17]
	ds_read_b128 v[174:177], v147 offset:6144
	ds_read_b128 v[182:185], v147 offset:7168
	s_waitcnt lgkmcnt(2)
	v_mfma_f32_16x16x32_bf16 v[14:17], v[178:181], v[186:189], v[14:17]
	ds_read_b128 v[178:181], v168 offset:96
	ds_read_b128 v[186:189], v168 offset:112
	s_waitcnt lgkmcnt(1)
	v_mfma_f32_16x16x32_bf16 v[14:17], v[174:177], v[178:181], v[14:17]
	s_waitcnt lgkmcnt(0)
	v_mfma_f32_16x16x32_bf16 v[14:17], v[182:185], v[186:189], v[14:17]
	ds_read_b128 v[174:177], v147 offset:8192
	ds_read_b128 v[178:181], v147 offset:9216
	ds_read_b128 v[182:185], v168 offset:128
	ds_read_b128 v[186:189], v168 offset:144
	s_waitcnt lgkmcnt(1)
	v_mfma_f32_16x16x32_bf16 v[14:17], v[174:177], v[182:185], v[14:17]
	ds_read_b128 v[174:177], v147 offset:10240
	ds_read_b128 v[182:185], v147 offset:11264
	s_waitcnt lgkmcnt(2)
	v_mfma_f32_16x16x32_bf16 v[14:17], v[178:181], v[186:189], v[14:17]
	ds_read_b128 v[178:181], v168 offset:160
	ds_read_b128 v[186:189], v168 offset:176
	s_waitcnt lgkmcnt(1)
	v_mfma_f32_16x16x32_bf16 v[14:17], v[174:177], v[178:181], v[14:17]
	s_waitcnt lgkmcnt(0)
	v_mfma_f32_16x16x32_bf16 v[14:17], v[182:185], v[186:189], v[14:17]
	ds_read_b128 v[174:177], v147 offset:12288
	ds_read_b128 v[178:181], v147 offset:13312
	ds_read_b128 v[182:185], v168 offset:192
	ds_read_b128 v[186:189], v168 offset:208
	s_waitcnt lgkmcnt(1)
	v_mfma_f32_16x16x32_bf16 v[14:17], v[174:177], v[182:185], v[14:17]
	ds_read_b128 v[174:177], v147 offset:14336
	ds_read_b128 v[182:185], v147 offset:15360
	s_waitcnt lgkmcnt(2)
	v_mfma_f32_16x16x32_bf16 v[14:17], v[178:181], v[186:189], v[14:17]
	ds_read_b128 v[178:181], v168 offset:224
	ds_read_b128 v[186:189], v168 offset:240
	s_waitcnt lgkmcnt(1)
	v_mfma_f32_16x16x32_bf16 v[14:17], v[174:177], v[178:181], v[14:17]
	s_waitcnt lgkmcnt(0)
	v_mfma_f32_16x16x32_bf16 v[14:17], v[182:185], v[186:189], v[14:17]
	s_waitcnt vmcnt(42)
	v_cmp_ne_u16_e64 s[22:23], -1, v172
	s_and_b64 s[22:23], s[20:21], s[22:23]
	s_and_saveexec_b64 s[20:21], s[22:23]
	v_and_b32_e32 v147, 0xffff, v172
	v_mov_b32_e32 v148, 0x18500
	v_lshl_add_u32 v147, v147, 2, v148
	v_mov_b32_e32 v148, 1
	ds_add_u32 v147, v148
	s_or_b64 exec, exec, s[20:21]
	v_mov_b32_e32 v147, 0xffff
	s_mov_b32 s22, 0xffff
	s_waitcnt vmcnt(41)
	v_cndmask_b32_sdwa v148, v147, v161, vcc dst_sel:DWORD dst_unused:UNUSED_PAD src0_sel:DWORD src1_sel:WORD_0
	v_cmp_ne_u32_e32 vcc, s22, v148
	s_and_saveexec_b64 s[20:21], vcc
	v_mov_b32_e32 v149, 0x18500
	v_lshl_add_u32 v148, v148, 2, v149
	v_mov_b32_e32 v149, 1
	ds_add_u32 v148, v149
	s_or_b64 exec, exec, s[20:21]
	s_mov_b64 vcc, s[16:17]
	s_waitcnt vmcnt(40)
	v_cndmask_b32_sdwa v147, v147, v160, vcc dst_sel:DWORD dst_unused:UNUSED_PAD src0_sel:DWORD src1_sel:WORD_0
	v_cmp_ne_u32_e32 vcc, s22, v147
	s_and_saveexec_b64 s[16:17], vcc
	v_mov_b32_e32 v148, 0x18500
	v_lshl_add_u32 v147, v147, 2, v148
	v_mov_b32_e32 v148, 1
	ds_add_u32 v147, v148
	s_or_b64 exec, exec, s[16:17]
	s_mov_b64 vcc, s[18:19]
	v_mov_b32_e32 v147, 0xffff
	s_mov_b32 s18, 0xffff
	s_waitcnt vmcnt(39)
	v_cndmask_b32_sdwa v148, v147, v159, vcc dst_sel:DWORD dst_unused:UNUSED_PAD src0_sel:DWORD src1_sel:WORD_0
	v_cmp_ne_u32_e32 vcc, s18, v148
	s_and_saveexec_b64 s[16:17], vcc
	v_mov_b32_e32 v149, 0x18500
	v_lshl_add_u32 v148, v148, 2, v149
	v_mov_b32_e32 v149, 1
	ds_add_u32 v148, v149
	s_or_b64 exec, exec, s[16:17]
	s_mov_b64 vcc, s[12:13]
	s_waitcnt vmcnt(38)
	v_cndmask_b32_sdwa v147, v147, v157, vcc dst_sel:DWORD dst_unused:UNUSED_PAD src0_sel:DWORD src1_sel:WORD_0
	v_cmp_ne_u32_e32 vcc, s18, v147
	s_and_saveexec_b64 s[12:13], vcc
	v_mov_b32_e32 v148, 0x18500
	v_lshl_add_u32 v147, v147, 2, v148
	v_mov_b32_e32 v148, 1
	ds_add_u32 v147, v148
	s_or_b64 exec, exec, s[12:13]
	s_mov_b64 vcc, s[14:15]
	v_mov_b32_e32 v147, 0xffff
	s_mov_b32 s14, 0xffff
	s_waitcnt vmcnt(37)
	v_cndmask_b32_sdwa v148, v147, v156, vcc dst_sel:DWORD dst_unused:UNUSED_PAD src0_sel:DWORD src1_sel:WORD_0
	v_cmp_ne_u32_e32 vcc, s14, v148
	s_and_saveexec_b64 s[12:13], vcc
	v_mov_b32_e32 v149, 0x18500
	v_lshl_add_u32 v148, v148, 2, v149
	v_mov_b32_e32 v149, 1
	ds_add_u32 v148, v149
	s_or_b64 exec, exec, s[12:13]
	s_mov_b64 vcc, s[10:11]
	s_waitcnt vmcnt(36)
	v_cndmask_b32_sdwa v147, v147, v155, vcc dst_sel:DWORD dst_unused:UNUSED_PAD src0_sel:DWORD src1_sel:WORD_0
	v_cmp_ne_u32_e32 vcc, s14, v147
	s_and_saveexec_b64 s[10:11], vcc
	v_mov_b32_e32 v148, 0x18500
	v_lshl_add_u32 v147, v147, 2, v148
	v_mov_b32_e32 v148, 1
	ds_add_u32 v147, v148
	s_or_b64 exec, exec, s[10:11]
	s_mov_b64 vcc, s[4:5]
	v_mov_b32_e32 v147, 0xffff
	s_mov_b32 s10, 0xffff
	s_waitcnt vmcnt(35)
	v_cndmask_b32_sdwa v148, v147, v153, vcc dst_sel:DWORD dst_unused:UNUSED_PAD src0_sel:DWORD src1_sel:WORD_0
	v_cmp_ne_u32_e32 vcc, s10, v148
	s_and_saveexec_b64 s[4:5], vcc
	v_mov_b32_e32 v149, 0x18500
	v_lshl_add_u32 v148, v148, 2, v149
	v_mov_b32_e32 v149, 1
	ds_add_u32 v148, v149
	s_or_b64 exec, exec, s[4:5]
	s_mov_b64 vcc, s[6:7]
	s_waitcnt vmcnt(34)
	v_cndmask_b32_sdwa v147, v147, v154, vcc dst_sel:DWORD dst_unused:UNUSED_PAD src0_sel:DWORD src1_sel:WORD_0
	v_cmp_ne_u32_e32 vcc, s10, v147
	s_and_saveexec_b64 s[4:5], vcc
	v_mov_b32_e32 v148, 0x18500
	v_lshl_add_u32 v147, v147, 2, v148
	v_mov_b32_e32 v148, 1
	ds_add_u32 v147, v148
	s_or_b64 exec, exec, s[4:5]
	s_mov_b64 vcc, s[8:9]
	v_mov_b32_e32 v147, 0xffff
	s_mov_b32 s6, 0xffff
	s_waitcnt vmcnt(33)
	v_cndmask_b32_sdwa v148, v147, v152, vcc dst_sel:DWORD dst_unused:UNUSED_PAD src0_sel:DWORD src1_sel:WORD_0
	v_cmp_ne_u32_e32 vcc, s6, v148
	s_and_saveexec_b64 s[4:5], vcc
	v_mov_b32_e32 v149, 0x18500
	v_lshl_add_u32 v148, v148, 2, v149
	v_mov_b32_e32 v149, 1
	ds_add_u32 v148, v149
	s_or_b64 exec, exec, s[4:5]
	s_mov_b64 vcc, s[0:1]
	s_waitcnt vmcnt(32)
	v_cndmask_b32_sdwa v147, v147, v151, vcc dst_sel:DWORD dst_unused:UNUSED_PAD src0_sel:DWORD src1_sel:WORD_0
	v_cmp_ne_u32_e32 vcc, s6, v147
	s_and_saveexec_b64 s[0:1], vcc
	v_mov_b32_e32 v148, 0x18500
	v_lshl_add_u32 v147, v147, 2, v148
	v_mov_b32_e32 v148, 1
	ds_add_u32 v147, v148
	s_or_b64 exec, exec, s[0:1]
	v_mov_b32_e32 v184, v1
	ds_read2_b32 v[148:149], v169 offset0:220 offset1:225
	ds_read2_b32 v[152:153], v170 offset0:220 offset1:225
	ds_read2_b32 v[154:155], v170 offset0:230 offset1:235
	ds_read2_b32 v[156:157], v169 offset0:230 offset1:235
	v_mov_b32_e32 v161, 0
	s_waitcnt lgkmcnt(3)
	v_add_u32_e32 v147, v148, v1
	s_waitcnt lgkmcnt(2)
	v_cmp_lt_u32_e64 s[20:21], v1, v152
	v_cmp_lt_u32_e32 vcc, v1, v153
	s_waitcnt lgkmcnt(1)
	v_cmp_lt_u32_e64 s[16:17], v1, v154
	v_cndmask_b32_e64 v160, 0, v147, s[20:21]
	v_add_u32_e32 v147, v149, v1
	v_lshl_add_u64 v[162:163], v[160:161], 1, s[26:27]
	v_cndmask_b32_e32 v160, 0, v147, vcc
	s_waitcnt lgkmcnt(0)
	v_add_u32_e32 v147, v156, v1
	v_lshl_add_u64 v[148:149], v[160:161], 1, s[26:27]
	v_cndmask_b32_e64 v160, 0, v147, s[16:17]
	v_add_u32_e32 v147, v157, v1
	ds_read2_b32 v[156:157], v169 offset0:240 offset1:245
	ds_read2_b32 v[172:173], v170 offset0:240 offset1:245
	v_cmp_lt_u32_e64 s[18:19], v1, v155
	v_lshl_add_u64 v[152:153], v[160:161], 1, s[26:27]
	s_waitcnt lgkmcnt(0)
	v_cmp_lt_u32_e64 s[12:13], v1, v172
	v_cndmask_b32_e64 v160, 0, v147, s[18:19]
	v_add_u32_e32 v147, v156, v1
	v_lshl_add_u64 v[154:155], v[160:161], 1, s[26:27]
	v_cndmask_b32_e64 v160, 0, v147, s[12:13]
	v_add_u32_e32 v147, v157, v1
	ds_read2_b32 v[156:157], v169 offset0:250 offset1:255
	ds_read2_b32 v[176:177], v170 offset0:250 offset1:255
	v_cmp_lt_u32_e64 s[14:15], v1, v173
	v_lshl_add_u64 v[174:175], v[160:161], 1, s[26:27]
	s_waitcnt lgkmcnt(0)
	v_cmp_lt_u32_e64 s[10:11], v1, v176
	v_cndmask_b32_e64 v160, 0, v147, s[14:15]
	v_add_u32_e32 v147, v156, v1
	v_lshl_add_u64 v[172:173], v[160:161], 1, s[26:27]
	v_cndmask_b32_e64 v160, 0, v147, s[10:11]
	v_add_u32_e32 v147, v157, v1
	v_cmp_lt_u32_e64 s[4:5], v1, v177
	v_lshl_add_u64 v[178:179], v[160:161], 1, s[26:27]
	s_nop 0
	v_cndmask_b32_e64 v160, 0, v147, s[4:5]
	v_add_u32_e32 v147, 0x400, v169
	ds_read2_b32 v[180:181], v147 offset0:4 offset1:9
	v_add_u32_e32 v147, 0x400, v170
	ds_read2_b32 v[182:183], v147 offset0:4 offset1:9
	v_lshl_add_u64 v[176:177], v[160:161], 1, s[26:27]
	global_load_ushort v159, v[162:163], off
	global_load_ushort v157, v[148:149], off
	global_load_ushort v156, v[152:153], off
	s_nop 0
	global_load_ushort v155, v[154:155], off
	s_nop 0
	global_load_ushort v154, v[174:175], off
	global_load_ushort v153, v[172:173], off
	global_load_ushort v152, v[178:179], off
	global_load_ushort v149, v[176:177], off
	ds_read_b32 v148, v169 offset:1080
	ds_read_b32 v151, v170 offset:1080
	s_waitcnt lgkmcnt(3)
	v_add_u32_e32 v147, v180, v1
	s_waitcnt lgkmcnt(2)
	v_cmp_lt_u32_e64 s[6:7], v1, v182
	v_cmp_lt_u32_e64 s[8:9], v1, v183
	s_waitcnt lgkmcnt(0)
	v_cmp_lt_u32_e64 s[0:1], v1, v151
	v_cndmask_b32_e64 v160, 0, v147, s[6:7]
	v_add_u32_e32 v147, v181, v1
	v_lshl_add_u64 v[162:163], v[160:161], 1, s[26:27]
	v_cndmask_b32_e64 v160, 0, v147, s[8:9]
	v_add_u32_e32 v147, v148, v1
	v_lshl_add_u64 v[172:173], v[160:161], 1, s[26:27]
	v_cndmask_b32_e64 v160, 0, v147, s[0:1]
	v_lshl_add_u64 v[160:161], v[160:161], 1, s[26:27]
	global_load_ushort v151, v[162:163], off
	global_load_ushort v148, v[172:173], off
	global_load_ushort v147, v[160:161], off
	s_waitcnt vmcnt(40)
	v_cvt_pk_bf16_f32 v102, v102, v103
	v_cvt_pk_bf16_f32 v103, v104, v105
	s_waitcnt vmcnt(39)
	v_cvt_pk_bf16_f32 v90, v90, v91
	v_cvt_pk_bf16_f32 v91, v92, v93
	ds_write2_b64 v171, v[102:103], v[90:91] offset0:130 offset1:194
	s_waitcnt vmcnt(28)
	v_cvt_pk_bf16_f32 v90, v126, v127
	v_cvt_pk_bf16_f32 v91, v128, v129
	v_cvt_pk_bf16_f32 v92, v106, v107
	v_cvt_pk_bf16_f32 v93, v108, v109
	v_add_u32_e32 v102, 32, v171
	v_cvt_pk_bf16_f32 v58, v58, v59
	v_cvt_pk_bf16_f32 v59, v60, v61
	v_cvt_pk_bf16_f32 v46, v46, v47
	v_cvt_pk_bf16_f32 v47, v48, v49
	v_add_u32_e32 v48, 0x50, v171
	v_cvt_pk_bf16_f32 v122, v122, v123
	v_cvt_pk_bf16_f32 v123, v124, v125
	v_cvt_pk_bf16_f32 v118, v118, v119
	v_cvt_pk_bf16_f32 v119, v120, v121
	ds_write2st64_b64 v102, v[90:91], v[92:93] offset0:4 offset1:5
	v_cvt_pk_bf16_f32 v78, v78, v79
	v_cvt_pk_bf16_f32 v79, v80, v81
	v_cvt_pk_bf16_f32 v80, v110, v111
	v_cvt_pk_bf16_f32 v81, v112, v113
	v_add_u32_e32 v90, 48, v171
	v_cvt_pk_bf16_f32 v74, v74, v75
	v_cvt_pk_bf16_f32 v75, v76, v77
	v_cvt_pk_bf16_f32 v62, v62, v63
	v_cvt_pk_bf16_f32 v63, v64, v65
	v_add_u32_e32 v64, 64, v171
	ds_write2st64_b64 v48, v[58:59], v[46:47] offset0:10 offset1:11
	v_cvt_pk_bf16_f32 v46, v54, v55
	v_cvt_pk_bf16_f32 v47, v56, v57
	v_cvt_pk_bf16_f32 v30, v30, v31
	v_cvt_pk_bf16_f32 v31, v32, v33
	v_add_u32_e32 v32, 0x60, v171
	v_cvt_pk_bf16_f32 v26, v26, v27
	v_cvt_pk_bf16_f32 v27, v28, v29
	s_waitcnt vmcnt(27)
	v_cvt_pk_bf16_f32 v22, v22, v23
	v_cvt_pk_bf16_f32 v23, v24, v25
	v_add_u32_e32 v24, 0x70, v171
	ds_write2st64_b64 v171, v[122:123], v[118:119] offset1:1
	ds_write2st64_b64 v90, v[78:79], v[80:81] offset0:6 offset1:7
	ds_write2st64_b64 v64, v[74:75], v[62:63] offset0:8 offset1:9
	ds_write2st64_b64 v32, v[46:47], v[30:31] offset0:12 offset1:13
	ds_write2st64_b64 v24, v[26:27], v[22:23] offset0:14 offset1:15
	s_waitcnt vmcnt(26)
	v_cvt_pk_bf16_f32 v22, v138, v139
	v_cvt_pk_bf16_f32 v23, v140, v141
	s_waitcnt vmcnt(25)
	v_cvt_pk_bf16_f32 v24, v134, v135
	v_cvt_pk_bf16_f32 v25, v136, v137
	v_add_u32_e32 v26, 0x80, v171
	ds_write2st64_b64 v26, v[22:23], v[24:25] offset0:16 offset1:17
	s_waitcnt vmcnt(24)
	v_cvt_pk_bf16_f32 v22, v130, v131
	v_cvt_pk_bf16_f32 v23, v132, v133
	s_waitcnt vmcnt(23)
	v_cvt_pk_bf16_f32 v24, v98, v99
	v_cvt_pk_bf16_f32 v25, v100, v101
	v_add_u32_e32 v26, 0x90, v171
	ds_write2st64_b64 v26, v[22:23], v[24:25] offset0:18 offset1:19
	s_waitcnt vmcnt(12)
	v_cvt_pk_bf16_f32 v22, v142, v143
	v_cvt_pk_bf16_f32 v23, v144, v145
	v_cvt_pk_bf16_f32 v24, v114, v115
	v_cvt_pk_bf16_f32 v25, v116, v117
	v_add_u32_e32 v26, 0xa0, v171
	ds_write2st64_b64 v26, v[22:23], v[24:25] offset0:20 offset1:21
	v_cvt_pk_bf16_f32 v22, v86, v87
	v_cvt_pk_bf16_f32 v23, v88, v89
	v_cvt_pk_bf16_f32 v24, v94, v95
	v_cvt_pk_bf16_f32 v25, v96, v97
	v_add_u32_e32 v26, 0xb0, v171
	ds_write2st64_b64 v26, v[22:23], v[24:25] offset0:22 offset1:23
	v_cvt_pk_bf16_f32 v22, v82, v83
	v_cvt_pk_bf16_f32 v23, v84, v85
	v_cvt_pk_bf16_f32 v24, v70, v71
	v_cvt_pk_bf16_f32 v25, v72, v73
	v_add_u32_e32 v26, 0xc0, v171
	ds_write2st64_b64 v26, v[22:23], v[24:25] offset0:24 offset1:25
	v_cvt_pk_bf16_f32 v22, v66, v67
	v_cvt_pk_bf16_f32 v23, v68, v69
	v_cvt_pk_bf16_f32 v24, v42, v43
	v_cvt_pk_bf16_f32 v25, v44, v45
	v_add_u32_e32 v26, 0xd0, v171
	ds_write2st64_b64 v26, v[22:23], v[24:25] offset0:26 offset1:27
	v_cvt_pk_bf16_f32 v22, v50, v51
	v_cvt_pk_bf16_f32 v23, v52, v53
	v_cvt_pk_bf16_f32 v24, v38, v39
	v_cvt_pk_bf16_f32 v25, v40, v41
	v_add_u32_e32 v26, 0xe0, v171
	ds_write2st64_b64 v26, v[22:23], v[24:25] offset0:28 offset1:29
	v_cvt_pk_bf16_f32 v22, v34, v35
	v_cvt_pk_bf16_f32 v23, v36, v37
	s_waitcnt vmcnt(11)
	v_cvt_pk_bf16_f32 v18, v18, v19
	v_cvt_pk_bf16_f32 v19, v20, v21
	v_add_u32_e32 v20, 0xf0, v171
	ds_write2st64_b64 v20, v[22:23], v[18:19] offset0:30 offset1:31
	v_mov_b32_e32 v18, 0x14500
	v_lshl_add_u32 v38, v184, 4, v18
	ds_read_b128 v[18:21], v38
	ds_read_b128 v[22:25], v38 offset:1024
	ds_read_b128 v[26:29], v168
	ds_read_b128 v[30:33], v168 offset:16
	s_waitcnt lgkmcnt(1)
	v_mfma_f32_16x16x32_bf16 v[18:21], v[18:21], v[26:29], 0
	ds_read_b128 v[26:29], v38 offset:2048
	ds_read_b128 v[34:37], v38 offset:3072
	s_waitcnt lgkmcnt(2)
	v_mfma_f32_16x16x32_bf16 v[18:21], v[22:25], v[30:33], v[18:21]
	ds_read_b128 v[22:25], v168 offset:32
	ds_read_b128 v[30:33], v168 offset:48
	s_waitcnt lgkmcnt(1)
	v_mfma_f32_16x16x32_bf16 v[18:21], v[26:29], v[22:25], v[18:21]
	s_waitcnt lgkmcnt(0)
	v_mfma_f32_16x16x32_bf16 v[18:21], v[34:37], v[30:33], v[18:21]
	ds_read_b128 v[22:25], v38 offset:4096
	ds_read_b128 v[26:29], v38 offset:5120
	ds_read_b128 v[30:33], v168 offset:64
	ds_read_b128 v[34:37], v168 offset:80
	s_waitcnt lgkmcnt(1)
	v_mfma_f32_16x16x32_bf16 v[18:21], v[22:25], v[30:33], v[18:21]
	ds_read_b128 v[22:25], v38 offset:6144
	ds_read_b128 v[30:33], v38 offset:7168
	s_waitcnt lgkmcnt(2)
	v_mfma_f32_16x16x32_bf16 v[18:21], v[26:29], v[34:37], v[18:21]
	ds_read_b128 v[26:29], v168 offset:96
	ds_read_b128 v[34:37], v168 offset:112
	s_waitcnt lgkmcnt(1)
	v_mfma_f32_16x16x32_bf16 v[18:21], v[22:25], v[26:29], v[18:21]
	s_waitcnt lgkmcnt(0)
	v_mfma_f32_16x16x32_bf16 v[18:21], v[30:33], v[34:37], v[18:21]
	ds_read_b128 v[22:25], v38 offset:8192
	ds_read_b128 v[26:29], v38 offset:9216
	ds_read_b128 v[30:33], v168 offset:128
	ds_read_b128 v[34:37], v168 offset:144
	s_waitcnt lgkmcnt(1)
	v_mfma_f32_16x16x32_bf16 v[18:21], v[22:25], v[30:33], v[18:21]
	ds_read_b128 v[22:25], v38 offset:10240
	ds_read_b128 v[30:33], v38 offset:11264
	s_waitcnt lgkmcnt(2)
	v_mfma_f32_16x16x32_bf16 v[18:21], v[26:29], v[34:37], v[18:21]
	ds_read_b128 v[26:29], v168 offset:160
	ds_read_b128 v[34:37], v168 offset:176
	s_waitcnt lgkmcnt(1)
	v_mfma_f32_16x16x32_bf16 v[18:21], v[22:25], v[26:29], v[18:21]
	s_waitcnt lgkmcnt(0)
	v_mfma_f32_16x16x32_bf16 v[18:21], v[30:33], v[34:37], v[18:21]
	ds_read_b128 v[22:25], v38 offset:12288
	ds_read_b128 v[26:29], v38 offset:13312
	ds_read_b128 v[30:33], v168 offset:192
	ds_read_b128 v[34:37], v168 offset:208
	s_waitcnt lgkmcnt(1)
	v_mfma_f32_16x16x32_bf16 v[18:21], v[22:25], v[30:33], v[18:21]
	ds_read_b128 v[22:25], v38 offset:14336
	ds_read_b128 v[30:33], v38 offset:15360
	s_waitcnt lgkmcnt(2)
	v_mfma_f32_16x16x32_bf16 v[18:21], v[26:29], v[34:37], v[18:21]
	ds_read_b128 v[26:29], v168 offset:224
	ds_read_b128 v[34:37], v168 offset:240
	s_waitcnt lgkmcnt(1)
	v_mfma_f32_16x16x32_bf16 v[18:21], v[22:25], v[26:29], v[18:21]
	s_waitcnt lgkmcnt(0)
	v_mfma_f32_16x16x32_bf16 v[18:21], v[30:33], v[34:37], v[18:21]
	s_waitcnt vmcnt(10)
	v_cmp_ne_u16_e64 s[22:23], -1, v159
	s_and_b64 s[22:23], s[20:21], s[22:23]
	s_and_saveexec_b64 s[20:21], s[22:23]
	v_and_b32_e32 v22, 0xffff, v159
	v_mov_b32_e32 v23, 0x18500
	v_lshl_add_u32 v22, v22, 2, v23
	v_mov_b32_e32 v23, 1
	ds_add_u32 v22, v23
	s_or_b64 exec, exec, s[20:21]
	v_mov_b32_e32 v22, 0xffff
	s_mov_b32 s22, 0xffff
	s_waitcnt vmcnt(9)
	v_cndmask_b32_sdwa v23, v22, v157, vcc dst_sel:DWORD dst_unused:UNUSED_PAD src0_sel:DWORD src1_sel:WORD_0
	v_cmp_ne_u32_e32 vcc, s22, v23
	s_and_saveexec_b64 s[20:21], vcc
	v_mov_b32_e32 v24, 0x18500
	v_lshl_add_u32 v23, v23, 2, v24
	v_mov_b32_e32 v24, 1
	ds_add_u32 v23, v24
	s_or_b64 exec, exec, s[20:21]
	s_mov_b64 vcc, s[16:17]
	s_waitcnt vmcnt(8)
	v_cndmask_b32_sdwa v22, v22, v156, vcc dst_sel:DWORD dst_unused:UNUSED_PAD src0_sel:DWORD src1_sel:WORD_0
	v_cmp_ne_u32_e32 vcc, s22, v22
	s_and_saveexec_b64 s[16:17], vcc
	v_mov_b32_e32 v23, 0x18500
	v_lshl_add_u32 v22, v22, 2, v23
	v_mov_b32_e32 v23, 1
	ds_add_u32 v22, v23
	s_or_b64 exec, exec, s[16:17]
	s_mov_b64 vcc, s[18:19]
	v_mov_b32_e32 v22, 0xffff
	s_mov_b32 s18, 0xffff
	s_waitcnt vmcnt(7)
	v_cndmask_b32_sdwa v23, v22, v155, vcc dst_sel:DWORD dst_unused:UNUSED_PAD src0_sel:DWORD src1_sel:WORD_0
	v_cmp_ne_u32_e32 vcc, s18, v23
	s_and_saveexec_b64 s[16:17], vcc
	v_mov_b32_e32 v24, 0x18500
	v_lshl_add_u32 v23, v23, 2, v24
	v_mov_b32_e32 v24, 1
	ds_add_u32 v23, v24
	s_or_b64 exec, exec, s[16:17]
	s_mov_b64 vcc, s[12:13]
	s_waitcnt vmcnt(6)
	v_cndmask_b32_sdwa v22, v22, v154, vcc dst_sel:DWORD dst_unused:UNUSED_PAD src0_sel:DWORD src1_sel:WORD_0
	v_cmp_ne_u32_e32 vcc, s18, v22
	s_and_saveexec_b64 s[12:13], vcc
	v_mov_b32_e32 v23, 0x18500
	v_lshl_add_u32 v22, v22, 2, v23
	v_mov_b32_e32 v23, 1
	ds_add_u32 v22, v23
	s_or_b64 exec, exec, s[12:13]
	s_mov_b64 vcc, s[14:15]
	v_mov_b32_e32 v22, 0xffff
	s_mov_b32 s14, 0xffff
	s_waitcnt vmcnt(5)
	v_cndmask_b32_sdwa v23, v22, v153, vcc dst_sel:DWORD dst_unused:UNUSED_PAD src0_sel:DWORD src1_sel:WORD_0
	v_cmp_ne_u32_e32 vcc, s14, v23
	s_and_saveexec_b64 s[12:13], vcc
	v_mov_b32_e32 v24, 0x18500
	v_lshl_add_u32 v23, v23, 2, v24
	v_mov_b32_e32 v24, 1
	ds_add_u32 v23, v24
	s_or_b64 exec, exec, s[12:13]
	s_mov_b64 vcc, s[10:11]
	s_waitcnt vmcnt(4)
	v_cndmask_b32_sdwa v22, v22, v152, vcc dst_sel:DWORD dst_unused:UNUSED_PAD src0_sel:DWORD src1_sel:WORD_0
	v_cmp_ne_u32_e32 vcc, s14, v22
	s_and_saveexec_b64 s[10:11], vcc
	v_mov_b32_e32 v23, 0x18500
	v_lshl_add_u32 v22, v22, 2, v23
	v_mov_b32_e32 v23, 1
	ds_add_u32 v22, v23
	s_or_b64 exec, exec, s[10:11]
	s_mov_b64 vcc, s[4:5]
	v_mov_b32_e32 v22, 0xffff
	s_mov_b32 s10, 0xffff
	s_waitcnt vmcnt(3)
	v_cndmask_b32_sdwa v23, v22, v149, vcc dst_sel:DWORD dst_unused:UNUSED_PAD src0_sel:DWORD src1_sel:WORD_0
	v_cmp_ne_u32_e32 vcc, s10, v23
	s_and_saveexec_b64 s[4:5], vcc
	v_mov_b32_e32 v24, 0x18500
	v_lshl_add_u32 v23, v23, 2, v24
	v_mov_b32_e32 v24, 1
	ds_add_u32 v23, v24
	s_or_b64 exec, exec, s[4:5]
	s_mov_b64 vcc, s[6:7]
	s_waitcnt vmcnt(2)
	v_cndmask_b32_sdwa v22, v22, v151, vcc dst_sel:DWORD dst_unused:UNUSED_PAD src0_sel:DWORD src1_sel:WORD_0
	v_cmp_ne_u32_e32 vcc, s10, v22
	s_and_saveexec_b64 s[4:5], vcc
	v_mov_b32_e32 v23, 0x18500
	v_lshl_add_u32 v22, v22, 2, v23
	v_mov_b32_e32 v23, 1
	ds_add_u32 v22, v23
	s_or_b64 exec, exec, s[4:5]
	s_mov_b64 vcc, s[8:9]
	v_mov_b32_e32 v22, 0xffff
	s_mov_b32 s6, 0xffff
	s_waitcnt vmcnt(1)
	v_cndmask_b32_sdwa v23, v22, v148, vcc dst_sel:DWORD dst_unused:UNUSED_PAD src0_sel:DWORD src1_sel:WORD_0
	v_cmp_ne_u32_e32 vcc, s6, v23
	s_and_saveexec_b64 s[4:5], vcc
	v_mov_b32_e32 v24, 0x18500
	v_lshl_add_u32 v23, v23, 2, v24
	v_mov_b32_e32 v24, 1
	ds_add_u32 v23, v24
	s_or_b64 exec, exec, s[4:5]
	s_mov_b64 vcc, s[0:1]
	s_waitcnt vmcnt(0)
	v_cndmask_b32_sdwa v22, v22, v147, vcc dst_sel:DWORD dst_unused:UNUSED_PAD src0_sel:DWORD src1_sel:WORD_0
	v_cmp_ne_u32_e32 vcc, s6, v22
	s_and_saveexec_b64 s[0:1], vcc
	v_mov_b32_e32 v23, 0x18500
	v_lshl_add_u32 v22, v22, 2, v23
	v_mov_b32_e32 v23, 1
	ds_add_u32 v22, v23
	s_or_b64 exec, exec, s[0:1]
	v_mov_b32_e32 v22, 0x19440
	s_waitcnt lgkmcnt(0)
	s_barrier
	ds_read_b32 v22, v22
	s_waitcnt lgkmcnt(0)
	v_cmp_ne_u32_e32 vcc, 0, v22
	s_cbranch_vccz .LBB1_162
	v_or_b32_e32 v1, 64, v1
	s_mov_b64 s[0:1], 0
	v_mov_b32_e32 v24, 0x18b40
	v_mov_b32_e32 v23, 0
	v_mov_b32_e32 v25, 1
	s_movk_i32 s8, 0xfa
	v_mov_b32_e32 v26, 0x18fc0
	v_mov_b32_e32 v27, 0x18500
	v_mov_b32_e32 v28, v164
	s_branch .LBB1_158

	.amdhsa_kernel _Z6k_gemmPKfS0_PKtPKjPfPt
		.amdhsa_group_segment_fixed_size 103492
		.amdhsa_private_segment_fixed_size 0
		.amdhsa_kernarg_size 48
		.amdhsa_user_sgpr_count 2
		.amdhsa_user_sgpr_dispatch_ptr 0
		.amdhsa_user_sgpr_queue_ptr 0
		.amdhsa_user_sgpr_kernarg_segment_ptr 1
		.amdhsa_user_sgpr_dispatch_id 0
		.amdhsa_user_sgpr_kernarg_preload_length 0
		.amdhsa_user_sgpr_kernarg_preload_offset 0
		.amdhsa_user_sgpr_private_segment_size 0
		.amdhsa_uses_dynamic_stack 0
		.amdhsa_enable_private_segment 0
		.amdhsa_system_sgpr_workgroup_id_x 1
		.amdhsa_system_sgpr_workgroup_id_y 0
		.amdhsa_system_sgpr_workgroup_id_z 0
		.amdhsa_system_sgpr_workgroup_info 0
		.amdhsa_system_vgpr_workitem_id 0
		.amdhsa_next_free_vgpr 192
		.amdhsa_next_free_sgpr 96
		.amdhsa_accum_offset 192
		.amdhsa_reserve_vcc 1
		.amdhsa_float_round_mode_32 0
		.amdhsa_float_round_mode_16_64 0
		.amdhsa_float_denorm_mode_32 3
		.amdhsa_float_denorm_mode_16_64 3
		.amdhsa_dx10_clamp 1
		.amdhsa_ieee_mode 1
		.amdhsa_fp16_overflow 0
		.amdhsa_tg_split 0
		.amdhsa_exception_fp_ieee_invalid_op 0
		.amdhsa_exception_fp_denorm_src 0
		.amdhsa_exception_fp_ieee_div_zero 0
		.amdhsa_exception_fp_ieee_overflow 0
		.amdhsa_exception_fp_ieee_underflow 0
		.amdhsa_exception_fp_ieee_inexact 0
		.amdhsa_exception_int_div_zero 0
	.end_amdhsa_kernel

.LBB2_2:
	s_or_b64 exec, exec, s[4:5]
	s_load_dwordx8 s[48:55], s[0:1], 0x30
	s_load_dwordx2 s[46:47], s[0:1], 0x0
	s_load_dwordx8 s[56:63], s[0:1], 0x10
	s_and_b32 s3, s2, 7
	s_mul_i32 s4, s3, 31
	s_min_u32 s3, s3, 2
	s_ashr_i32 s2, s2, 3
	v_and_b32_e32 v45, 63, v0
	s_add_i32 s64, s3, s2
	v_lshrrev_b32_e32 v6, 6, v0
	s_add_i32 s64, s64, s4
	v_cmp_gt_u32_e64 s[4:5], 16, v45
	v_mov_b32_e32 v4, 0
	v_mov_b32_e32 v2, 0
	v_mov_b32_e32 v3, 0
	s_load_dwordx2 s[6:7], s[0:1], 0x8
	v_lshlrev_b32_e32 v50, 2, v0
	s_movk_i32 s2, 0x280
	v_cmp_gt_u32_e32 vcc, s2, v0
	s_waitcnt lgkmcnt(0)
	s_and_saveexec_b64 s[2:3], vcc
	s_cbranch_execz .Lpro_a
	global_load_dword v100, v50, s[48:49]
.Lpro_a:
	s_or_b64 exec, exec, s[2:3]
	v_cmp_gt_u32_e32 vcc, 40, v0
	s_and_saveexec_b64 s[2:3], vcc
	s_cbranch_execz .Lpro_b
	global_load_dword v101, v50, s[50:51]
.Lpro_b:
	s_or_b64 exec, exec, s[2:3]
	s_and_saveexec_b64 s[2:3], s[4:5]
	s_cbranch_execz .LBB2_4
	v_lshl_or_b32 v102, v6, 4, v45
	s_movk_i32 s8, 0x101
	v_mov_b32_e32 v2, s64
	v_mad_u32_u24 v2, v102, s8, v2
	v_ashrrev_i32_e32 v3, 31, v2
	v_lshl_add_u64 v[2:3], v[2:3], 2, s[6:7]
	global_load_dwordx2 v[2:3], v[2:3], off

.LBB2_10:
	s_or_b64 exec, exec, s[8:9]
	s_movk_i32 s2, 0x280
	v_cmp_gt_u32_e32 vcc, s2, v0
	s_waitcnt vmcnt(0)
	s_and_saveexec_b64 s[2:3], vcc
	v_add_u32_e32 v5, 0x16400, v50
	ds_write_b32 v5, v100
.LBB2_12:
	s_or_b64 exec, exec, s[2:3]
	v_cmp_gt_u32_e32 vcc, 40, v0
	s_and_saveexec_b64 s[2:3], vcc
	v_add_u32_e32 v5, 0x17c50, v50
	ds_write_b32 v5, v101
.LBB2_14:
	s_or_b64 exec, exec, s[2:3]
	s_and_saveexec_b64 s[2:3], s[4:5]
	s_movk_i32 s6, 0x30d4
	v_lshlrev_b32_e32 v5, 2, v102
	v_add_u32_e32 v7, 0x17850, v5
	v_add_u32_e32 v5, 0x17450, v5
	v_mad_u32_u24 v1, v102, s6, v2
	v_sub_u32_e32 v8, v3, v2
	ds_write_b32 v7, v1
	ds_write_b32 v5, v8
	s_or_b64 exec, exec, s[2:3]
	v_readlane_b32 s2, v2, 0
	v_readlane_b32 s3, v3, 0
	v_mul_u32_u24_e32 v4, 0x30d40, v6
	s_sub_i32 s42, s3, s2
	v_or_b32_e32 v4, v4, v45
	v_add_u32_e32 v4, s2, v4
	v_cmp_gt_u32_e64 s[20:21], s42, v45
	v_lshlrev_b32_e32 v48, 4, v6
	v_mov_b32_e32 v5, 0
	v_cndmask_b32_e64 v4, 0, v4, s[20:21]
	v_readlane_b32 s2, v2, 1
	v_readlane_b32 s3, v3, 1
	s_waitcnt lgkmcnt(0)
	v_lshl_add_u64 v[20:21], v[4:5], 2, s[46:47]
	v_or_b32_e32 v4, 1, v48
	s_sub_i32 s50, s3, s2
	s_movk_i32 s3, 0x30d4
	v_mad_u32_u24 v10, v4, s3, v45
	v_add_u32_e32 v4, s2, v10
	v_cmp_gt_u32_e64 s[8:9], s50, v45
	v_readlane_b32 s2, v2, 2
	v_readlane_b32 s3, v3, 2
	v_cndmask_b32_e64 v4, 0, v4, s[8:9]
	s_sub_i32 s48, s3, s2
	v_add_u32_e32 v7, 0x30d4, v10
	v_lshl_add_u64 v[22:23], v[4:5], 2, s[46:47]
	v_add_u32_e32 v4, s2, v7
	v_cmp_gt_u32_e64 s[10:11], s48, v45
	v_readlane_b32 s2, v2, 3
	v_readlane_b32 s3, v3, 3
	v_cndmask_b32_e64 v4, 0, v4, s[10:11]
	v_lshl_add_u64 v[24:25], v[4:5], 2, s[46:47]
	s_sub_i32 s43, s3, s2
	v_add_u32_e32 v4, s2, v7
	v_add_u32_e32 v4, 0x30d4, v4
	v_cmp_gt_u32_e64 s[12:13], s43, v45
	v_readlane_b32 s2, v2, 4
	v_readlane_b32 s3, v3, 4
	v_cndmask_b32_e64 v4, 0, v4, s[12:13]
	s_sub_i32 s51, s3, s2
	v_add_u32_e32 v7, 0x927c, v10
	v_lshl_add_u64 v[26:27], v[4:5], 2, s[46:47]
	v_add_u32_e32 v4, s2, v7
	v_cmp_gt_u32_e64 s[14:15], s51, v45
	v_readlane_b32 s2, v2, 5
	v_readlane_b32 s3, v3, 5
	v_cndmask_b32_e64 v4, 0, v4, s[14:15]
	v_lshl_add_u64 v[28:29], v[4:5], 2, s[46:47]
	s_sub_i32 s49, s3, s2
	v_add_u32_e32 v4, s2, v7
	v_add_u32_e32 v4, 0x30d4, v4
	v_cmp_gt_u32_e64 s[16:17], s49, v45
	v_readlane_b32 s2, v2, 6
	v_readlane_b32 s3, v3, 6
	v_cndmask_b32_e64 v4, 0, v4, s[16:17]
	s_sub_i32 s66, s3, s2
	v_add_u32_e32 v7, 0xf424, v10
	v_lshl_add_u64 v[30:31], v[4:5], 2, s[46:47]
	v_add_u32_e32 v4, s2, v7
	v_cmp_gt_u32_e64 s[18:19], s66, v45
	v_readlane_b32 s2, v2, 7
	v_readlane_b32 s3, v3, 7
	v_cndmask_b32_e64 v4, 0, v4, s[18:19]
	v_lshl_add_u64 v[32:33], v[4:5], 2, s[46:47]
	s_sub_i32 s65, s3, s2
	v_add_u32_e32 v4, s2, v7
	v_add_u32_e32 v4, 0x30d4, v4
	v_cmp_gt_u32_e64 s[22:23], s65, v45
	v_readlane_b32 s2, v2, 8
	v_readlane_b32 s3, v3, 8
	v_cndmask_b32_e64 v4, 0, v4, s[22:23]
	s_sub_i32 s68, s3, s2
	v_add_u32_e32 v12, 0x155cc, v10
	v_lshl_add_u64 v[34:35], v[4:5], 2, s[46:47]
	v_add_u32_e32 v4, s2, v12
	v_cmp_gt_u32_e64 s[24:25], s68, v45
	v_readlane_b32 s2, v2, 9
	v_readlane_b32 s3, v3, 9
	v_cndmask_b32_e64 v4, 0, v4, s[24:25]
	global_load_dword v18, v[20:21], off
	global_load_dword v16, v[22:23], off
	global_load_dword v14, v[24:25], off
	global_load_dword v13, v[26:27], off
	global_load_dword v11, v[28:29], off
	global_load_dword v9, v[30:31], off
	global_load_dword v8, v[32:33], off
	global_load_dword v7, v[34:35], off
	v_lshl_add_u64 v[20:21], v[4:5], 2, s[46:47]
	s_sub_i32 s67, s3, s2
	v_add_u32_e32 v4, s2, v12
	v_add_u32_e32 v4, 0x30d4, v4
	v_cmp_gt_u32_e64 s[26:27], s67, v45
	v_readlane_b32 s2, v2, 10
	v_readlane_b32 s3, v3, 10
	v_cndmask_b32_e64 v4, 0, v4, s[26:27]
	s_sub_i32 s70, s3, s2
	v_add_u32_e32 v12, 0x1b774, v10
	v_lshl_add_u64 v[22:23], v[4:5], 2, s[46:47]
	v_add_u32_e32 v4, s2, v12
	v_cmp_gt_u32_e64 s[28:29], s70, v45
	v_readlane_b32 s2, v2, 11
	v_readlane_b32 s3, v3, 11
	v_cndmask_b32_e64 v4, 0, v4, s[28:29]
	v_lshl_add_u64 v[24:25], v[4:5], 2, s[46:47]
	s_sub_i32 s69, s3, s2
	v_add_u32_e32 v4, s2, v12
	v_add_u32_e32 v4, 0x30d4, v4
	v_cmp_gt_u32_e64 s[30:31], s69, v45
	v_readlane_b32 s2, v2, 12
	v_readlane_b32 s3, v3, 12
	v_cndmask_b32_e64 v4, 0, v4, s[30:31]
	s_sub_i32 s72, s3, s2
	v_add_u32_e32 v12, 0x2191c, v10
	v_lshl_add_u64 v[26:27], v[4:5], 2, s[46:47]
	v_add_u32_e32 v4, s2, v12
	v_cmp_gt_u32_e64 s[34:35], s72, v45
	v_readlane_b32 s2, v2, 13
	v_readlane_b32 s3, v3, 13
	v_cndmask_b32_e64 v4, 0, v4, s[34:35]
	v_lshl_add_u64 v[28:29], v[4:5], 2, s[46:47]
	s_sub_i32 s71, s3, s2
	v_add_u32_e32 v4, s2, v12
	v_add_u32_e32 v4, 0x30d4, v4
	v_cmp_gt_u32_e64 s[36:37], s71, v45
	v_readlane_b32 s2, v2, 14
	v_readlane_b32 s3, v3, 14
	v_cndmask_b32_e64 v4, 0, v4, s[36:37]
	v_add_u32_e32 v10, 0x27ac4, v10
	v_lshl_add_u64 v[30:31], v[4:5], 2, s[46:47]
	s_sub_i32 s74, s3, s2
	v_add_u32_e32 v4, s2, v10
	v_readlane_b32 s2, v2, 15
	v_readlane_b32 s3, v3, 15
	v_cmp_gt_u32_e64 s[6:7], s74, v45
	s_sub_i32 s73, s3, s2
	v_add_u32_e32 v2, s2, v10
	v_cndmask_b32_e64 v4, 0, v4, s[6:7]
	v_add_u32_e32 v2, 0x30d4, v2
	v_cmp_gt_u32_e32 vcc, s73, v45
	v_lshl_add_u64 v[32:33], v[4:5], 2, s[46:47]
	s_nop 0
	v_cndmask_b32_e32 v4, 0, v2, vcc
	v_lshl_add_u64 v[34:35], v[4:5], 2, s[46:47]
	global_load_dword v17, v[20:21], off
	global_load_dword v15, v[22:23], off
	global_load_dword v12, v[24:25], off
	global_load_dword v10, v[26:27], off
	global_load_dword v5, v[28:29], off
	global_load_dword v4, v[30:31], off
	global_load_dword v3, v[32:33], off
	global_load_dword v2, v[34:35], off
	s_barrier
	s_getreg_b32 s2, hwreg(HW_REG_XCC_ID, 0, 4)
	s_and_b32 s33, s2, 15
	s_and_saveexec_b64 s[38:39], s[44:45]
	s_cbranch_execz .LBB2_17
	s_mov_b64 s[40:41], exec
	v_mbcnt_lo_u32_b32 v19, s40, 0
	v_mbcnt_hi_u32_b32 v19, s41, v19
	v_cmp_eq_u32_e64 s[2:3], 0, v19
	s_and_b64 s[2:3], exec, s[2:3]
	s_mov_b64 exec, s[2:3]
	s_cbranch_execz .LBB2_17
	s_lshl_b32 s2, s33, 8
	s_bcnt1_i32_b64 s3, s[40:41]
	v_mov_b32_e32 v19, s2
	v_mov_b32_e32 v20, s3
	global_atomic_add v19, v20, s[54:55] offset:1024

.LBB2_265:
	s_mulk_i32 s64, 0x190
	v_lshrrev_b32_e32 v2, 1, v0
	s_movk_i32 s2, 0x320
	v_cmp_gt_u32_e32 vcc, s2, v0
	v_add_u32_e32 v64, s64, v2
	s_mov_b32 s2, 0x186a0
	v_cmp_gt_i32_e64 s[2:3], s2, v64
	s_and_b64 s[8:9], vcc, s[2:3]
	v_mov_b32_e32 v46, 0
	v_mov_b32_e32 v47, 0
	s_and_saveexec_b64 s[2:3], s[8:9]
	v_mov_b32_e32 v3, 0x16e00
	v_lshl_add_u32 v2, v2, 2, v3
	ds_read2_b32 v[46:47], v2 offset1:1
	s_or_b64 exec, exec, s[2:3]
	s_waitcnt lgkmcnt(0)
	v_sub_u32_e32 v2, v47, v46
	v_cvt_f32_u32_e32 v2, v2
	v_and_b32_e32 v44, 1, v0
	v_max_f32_e32 v2, 1.0, v2
	v_rsq_f32_e32 v53, v2
	s_and_saveexec_b64 s[10:11], s[8:9]
	s_cbranch_execz .LBB2_285
	v_lshlrev_b32_e32 v109, 5, v44
	global_load_dwordx4 v[100:103], v109, s[60:61]
	global_load_dwordx4 v[104:107], v109, s[60:61] offset:16
	v_ashrrev_i32_e32 v65, 31, v64
	v_lshl_add_u64 v[110:111], v[64:65], 2, s[58:59]
	global_load_dword v108, v[110:111], off
	s_and_b64 vcc, exec, s[4:5]
	s_cbranch_vccz .LBB2_282
	v_add_u32_e32 v2, 8, v46
	v_mov_b32_e32 v55, 0x3f80
	v_mov_b32_e32 v54, 1.0
	v_cmp_le_u32_e32 vcc, v2, v47
	v_mov_b32_e32 v5, 0
	v_mov_b32_e32 v4, 0
	v_mov_b32_e32 v3, 0
	v_mov_b32_e32 v2, 0
	v_mov_b32_e32 v9, 0
	v_mov_b32_e32 v8, 0
	v_mov_b32_e32 v7, 0
	v_mov_b32_e32 v6, 0
	v_mov_b32_e32 v57, v46
	s_and_saveexec_b64 s[2:3], vcc
	s_cbranch_execz .LBB2_273
	v_mov_b32_e32 v5, 0
	v_mov_b32_e32 v43, v44
	v_lshlrev_b32_e32 v56, 2, v46
	s_mov_b64 s[12:13], 0
	v_mov_b32_e32 v57, v46
	v_mov_b32_e32 v4, v5
	v_mov_b32_e32 v3, v5
	v_mov_b32_e32 v2, v5
	v_mov_b32_e32 v9, v5
	v_mov_b32_e32 v8, v5
	v_mov_b32_e32 v7, v5
	v_mov_b32_e32 v6, v5

.LBB2_284:
	v_lshlrev_b64 v[22:23], 5, v[64:65]
	v_lshlrev_b32_e32 v20, 4, v44
	v_mov_b32_e32 v21, 0
	v_lshl_add_u64 v[22:23], s[62:63], 0, v[22:23]
	s_waitcnt vmcnt(0) lgkmcnt(0)
	v_fma_f32 v6, v53, v6, v100
	v_fma_f32 v7, v53, v7, v101
	v_fma_f32 v8, v53, v8, v102
	v_fma_f32 v13, v53, v9, v103
	v_fma_f32 v9, v53, v2, v104
	v_fma_f32 v10, v53, v3, v105
	v_fma_f32 v11, v53, v4, v106
	v_fma_f32 v17, v53, v5, v107
	v_max_f32_e32 v2, 0, v6
	v_max_f32_e32 v3, 0, v7
	v_max_f32_e32 v4, 0, v8
	v_max_f32_e32 v5, 0, v13
	v_max_f32_e32 v6, 0, v9
	v_max_f32_e32 v7, 0, v10
	v_max_f32_e32 v8, 0, v11
	v_max_f32_e32 v9, 0, v17
	v_pk_mul_f32 v[2:3], v[108:109], v[2:3] op_sel_hi:[0,1]
	v_pk_mul_f32 v[4:5], v[108:109], v[4:5] op_sel_hi:[0,1]
	v_pk_mul_f32 v[6:7], v[108:109], v[6:7] op_sel_hi:[0,1]
	v_pk_mul_f32 v[8:9], v[108:109], v[8:9] op_sel_hi:[0,1]
	v_cvt_pk_bf16_f32 v2, v2, v3
	v_cvt_pk_bf16_f32 v3, v4, v5
	v_cvt_pk_bf16_f32 v4, v6, v7
	v_cvt_pk_bf16_f32 v5, v8, v9
	v_lshl_add_u64 v[6:7], v[22:23], 0, v[20:21]
	global_store_dwordx4 v[6:7], v[2:5], off

amdhsa.kernels:
  - .agpr_count:     0
    .args:
      - .actual_access:  read_only
        .address_space:  global
        .offset:         0
        .size:           8
        .value_kind:     global_buffer
      - .actual_access:  read_only
        .address_space:  global
        .offset:         8
        .size:           8
        .value_kind:     global_buffer
      - .actual_access:  write_only
        .address_space:  global
        .offset:         16
        .size:           8
        .value_kind:     global_buffer
      - .actual_access:  write_only
        .address_space:  global
        .offset:         24
        .size:           8
        .value_kind:     global_buffer
      - .actual_access:  write_only
        .address_space:  global
        .offset:         32
        .size:           8
        .value_kind:     global_buffer
      - .actual_access:  write_only
        .address_space:  global
        .offset:         40
        .size:           8
        .value_kind:     global_buffer
      - .actual_access:  write_only
        .address_space:  global
        .offset:         48
        .size:           8
        .value_kind:     global_buffer
    .group_segment_fixed_size: 107840
    .kernarg_segment_align: 8
    .kernarg_segment_size: 56
    .language:       OpenCL C
    .language_version:
      - 2
      - 0
    .max_flat_workgroup_size: 1024
    .name:           _Z6k_partPKiS0_PjPtS1_S1_S1_
    .private_segment_fixed_size: 0
    .sgpr_count:     50
    .sgpr_spill_count: 0
    .symbol:         _Z6k_partPKiS0_PjPtS1_S1_S1_.kd
    .uniform_work_group_size: 1
    .uses_dynamic_stack: false
    .vgpr_count:     97
    .vgpr_spill_count: 0
    .wavefront_size: 64
  - .agpr_count:     0
    .args:
      - .actual_access:  read_only
        .address_space:  global
        .offset:         0
        .size:           8
        .value_kind:     global_buffer
      - .actual_access:  read_only
        .address_space:  global
        .offset:         8
        .size:           8
        .value_kind:     global_buffer
      - .actual_access:  read_only
        .address_space:  global
        .offset:         16
        .size:           8
        .value_kind:     global_buffer
      - .actual_access:  read_only
        .address_space:  global
        .offset:         24
        .size:           8
        .value_kind:     global_buffer
      - .actual_access:  write_only
        .address_space:  global
        .offset:         32
        .size:           8
        .value_kind:     global_buffer
      - .actual_access:  write_only
        .address_space:  global
        .offset:         40
        .size:           8
        .value_kind:     global_buffer
    .group_segment_fixed_size: 103492
    .kernarg_segment_align: 8
    .kernarg_segment_size: 48
    .language:       OpenCL C
    .language_version:
      - 2
      - 0
    .max_flat_workgroup_size: 320
    .name:           _Z6k_gemmPKfS0_PKtPKjPfPt
    .private_segment_fixed_size: 0
    .sgpr_count:     43
    .sgpr_spill_count: 0
    .symbol:         _Z6k_gemmPKfS0_PKtPKjPfPt.kd
    .uniform_work_group_size: 1
    .uses_dynamic_stack: false
    .vgpr_count:     192
    .vgpr_spill_count: 0
    .wavefront_size: 64
  - .agpr_count:     0
    .args:
      - .actual_access:  read_only
        .address_space:  global
        .offset:         0
        .size:           8
        .value_kind:     global_buffer
      - .actual_access:  read_only
        .address_space:  global
        .offset:         8
        .size:           8
        .value_kind:     global_buffer
      - .actual_access:  read_only
        .address_space:  global
        .offset:         16
        .size:           8
        .value_kind:     global_buffer
      - .actual_access:  read_only
        .address_space:  global
        .offset:         24
        .size:           8
        .value_kind:     global_buffer
      - .actual_access:  read_only
        .address_space:  global
        .offset:         32
        .size:           8
        .value_kind:     global_buffer
      - .address_space:  global
        .offset:         40
        .size:           8
        .value_kind:     global_buffer
      - .actual_access:  read_only
        .address_space:  global
        .offset:         48
        .size:           8
        .value_kind:     global_buffer
      - .actual_access:  read_only
        .address_space:  global
        .offset:         56
        .size:           8
        .value_kind:     global_buffer
      - .actual_access:  write_only
        .address_space:  global
        .offset:         64
        .size:           8
        .value_kind:     global_buffer
      - .address_space:  global
        .offset:         72
        .size:           8
        .value_kind:     global_buffer
      - .offset:         80
        .size:           4
        .value_kind:     hidden_block_count_x
      - .offset:         84
        .size:           4
        .value_kind:     hidden_block_count_y
      - .offset:         88
        .size:           4
        .value_kind:     hidden_block_count_z
      - .offset:         92
        .size:           2
        .value_kind:     hidden_group_size_x
      - .offset:         94
        .size:           2
        .value_kind:     hidden_group_size_y
      - .offset:         96
        .size:           2
        .value_kind:     hidden_group_size_z
      - .offset:         98
        .size:           2
        .value_kind:     hidden_remainder_x
      - .offset:         100
        .size:           2
        .value_kind:     hidden_remainder_y
      - .offset:         102
        .size:           2
        .value_kind:     hidden_remainder_z
      - .offset:         120
        .size:           8
        .value_kind:     hidden_global_offset_x
      - .offset:         128
        .size:           8
        .value_kind:     hidden_global_offset_y
      - .offset:         136
        .size:           8
        .value_kind:     hidden_global_offset_z
      - .offset:         144
        .size:           2
        .value_kind:     hidden_grid_dims
    .group_segment_fixed_size: 97600
    .kernarg_segment_align: 8
    .kernarg_segment_size: 336
    .language:       OpenCL C
    .language_version:
      - 2
      - 0
    .max_flat_workgroup_size: 1024
    .name:           _Z6k_aggfPKjS0_PKtPKfS4_PtS4_S4_PfPj
    .private_segment_fixed_size: 0
    .sgpr_count:     81
    .sgpr_spill_count: 0
    .symbol:         _Z6k_aggfPKjS0_PKtPKfS4_PtS4_S4_PfPj.kd
    .uniform_work_group_size: 1
    .uses_dynamic_stack: false
    .vgpr_count:     128
    .vgpr_spill_count: 0
    .wavefront_size: 64
